# routed-expert MFMA blocks: fp8->bf16 operand conversion by one exact v_cvt_scalef32_pk_bf16_fp8 (scale 1.0) instead of cvt_pk_f32_fp8 + cvt_pk_bf16_f32, 144 pairs
# speedup vs baseline: 1.0161x; 1.0024x over previous
.Lgx_es:
	s_waitcnt vmcnt(10)
	v_cvt_pk_bf16_f32 v2, v160, v164
	v_cvt_pk_bf16_f32 v3, v168, v172
	s_or_b32 s25, s42, s25
	s_waitcnt lgkmcnt(0)
	s_barrier
	ds_write2_b32 v0, v2, v3 offset1:8
	v_cvt_pk_bf16_f32 v2, v161, v165
	v_cvt_pk_bf16_f32 v3, v169, v173
	v_add_u32_e32 v4, 0x400, v0
	s_add_u32 s42, s67, s25
	ds_write2_b32 v4, v2, v3 offset0:32 offset1:40
	v_cvt_pk_bf16_f32 v2, v162, v166
	v_cvt_pk_bf16_f32 v3, v170, v174
	v_add_u32_e32 v4, 0x800, v0
	s_addc_u32 s43, s38, 0
	ds_write2_b32 v4, v2, v3 offset0:64 offset1:72
	v_cvt_pk_bf16_f32 v2, v163, v167
	v_cvt_pk_bf16_f32 v3, v171, v175
	v_add_u32_e32 v0, 0xc00, v0
	s_add_u32 s46, s42, 0x4000
	ds_write2_b32 v0, v2, v3 offset0:96 offset1:104
	s_addc_u32 s47, s43, 0
	v_mov_b32_e32 v0, v238
	global_load_dwordx4 v[160:163], v0, s[42:43] nt
	global_load_dwordx4 v[164:167], v0, s[42:43] offset:1024 nt
	global_load_dwordx4 v[168:171], v0, s[46:47] nt
	global_load_dwordx4 v[172:175], v0, s[46:47] offset:1024 nt
	s_add_i32 s25, s49, 0xffffff80
	s_and_b32 s25, s25, 0x380
	s_or_b32 s25, s25, 64
	s_add_u32 s46, s25, s54
	v_cndmask_b32_e64 v0, 0, 1, s[0:1]
	s_addc_u32 s47, 0, s55
	s_mul_i32 s90, s2, 0x4800
	v_cmp_ne_u32_e64 s[42:43], 1, v0
	s_andn2_b64 vcc, exec, s[0:1]
	s_cbranch_vccnz .LBB0_1308
	s_waitcnt vmcnt(8)
	v_add_u32_e32 v0, s90, v245
	ds_read_b128 v[2:5], v0
	v_cvt_scalef32_pk_bf16_fp8 v6, v212, 1.0
	v_cvt_scalef32_pk_bf16_fp8 v7, v212, 1.0 op_sel:[1,0,0]
	v_cvt_scalef32_pk_bf16_fp8 v8, v213, 1.0
	v_cvt_scalef32_pk_bf16_fp8 v9, v213, 1.0 op_sel:[1,0,0]
	ds_read_b128 v[10:13], v0 offset:4608
	ds_read_b128 v[248:251], v0 offset:9216
	ds_read_b128 v[216:219], v0 offset:13824
	s_waitcnt lgkmcnt(3)
	v_mfma_f32_32x32x16_bf16 v[144:159], v[2:5], v[6:9], v[144:159]
	s_waitcnt vmcnt(6)
	v_cvt_pk_f32_fp8_e32 v[14:15], v209
	s_waitcnt lgkmcnt(2)
	v_mfma_f32_32x32x16_bf16 v[112:127], v[10:13], v[6:9], v[112:127]
	s_waitcnt lgkmcnt(1)
	v_mfma_f32_32x32x16_bf16 v[128:143], v[248:251], v[6:9], v[128:143]
	s_waitcnt lgkmcnt(0)
	v_mfma_f32_32x32x16_bf16 v[96:111], v[216:219], v[6:9], v[96:111]
	v_cvt_pk_f32_fp8_e32 v[6:7], v208
	v_cvt_pk_f32_fp8_sdwa v[8:9], v208 src0_sel:WORD_1
	v_cvt_pk_f32_fp8_sdwa v[208:209], v209 src0_sel:WORD_1
	v_cvt_pk_bf16_f32 v6, v6, v7
	v_cvt_pk_bf16_f32 v7, v8, v9
	v_cvt_pk_bf16_f32 v8, v14, v15
	v_cvt_pk_bf16_f32 v9, v208, v209
	s_nop 1
	v_mfma_f32_32x32x16_bf16 v[80:95], v[2:5], v[6:9], v[80:95]
	ds_read_b128 v[2:5], v0 offset:16
	v_mfma_f32_32x32x16_bf16 v[48:63], v[10:13], v[6:9], v[48:63]
	v_cvt_pk_f32_fp8_e32 v[10:11], v215
	v_cvt_pk_f32_fp8_sdwa v[12:13], v215 src0_sel:WORD_1
	v_mfma_f32_32x32x16_bf16 v[64:79], v[248:251], v[6:9], v[64:79]
	v_mfma_f32_32x32x16_bf16 v[32:47], v[216:219], v[6:9], v[32:47]
	v_cvt_pk_f32_fp8_e32 v[6:7], v214
	v_cvt_pk_f32_fp8_sdwa v[8:9], v214 src0_sel:WORD_1
	ds_read_b128 v[212:215], v0 offset:9232
	ds_read_b128 v[216:219], v0 offset:13840
	v_cvt_pk_bf16_f32 v6, v6, v7
	v_cvt_pk_bf16_f32 v7, v8, v9
	v_cvt_pk_bf16_f32 v8, v10, v11
	v_cvt_pk_bf16_f32 v9, v12, v13
	ds_read_b128 v[10:13], v0 offset:4624
	s_waitcnt lgkmcnt(3)
	v_mfma_f32_32x32x16_bf16 v[144:159], v[2:5], v[6:9], v[144:159]
	s_waitcnt lgkmcnt(0)
	v_mfma_f32_32x32x16_bf16 v[112:127], v[10:13], v[6:9], v[112:127]
	v_mfma_f32_32x32x16_bf16 v[128:143], v[212:215], v[6:9], v[128:143]
	v_mfma_f32_32x32x16_bf16 v[96:111], v[216:219], v[6:9], v[96:111]
	v_cvt_scalef32_pk_bf16_fp8 v6, v210, 1.0
	v_cvt_scalef32_pk_bf16_fp8 v7, v210, 1.0 op_sel:[1,0,0]
	v_cvt_scalef32_pk_bf16_fp8 v8, v211, 1.0
	v_cvt_scalef32_pk_bf16_fp8 v9, v211, 1.0 op_sel:[1,0,0]
	ds_read_b128 v[208:211], v0 offset:9248
	v_cvt_pk_f32_fp8_e32 v[14:15], v193
	v_mfma_f32_32x32x16_bf16 v[80:95], v[2:5], v[6:9], v[80:95]
	ds_read_b128 v[2:5], v0 offset:32
	v_mfma_f32_32x32x16_bf16 v[48:63], v[10:13], v[6:9], v[48:63]
	v_mfma_f32_32x32x16_bf16 v[64:79], v[212:215], v[6:9], v[64:79]
	ds_read_b128 v[212:215], v0 offset:13856
	v_mfma_f32_32x32x16_bf16 v[32:47], v[216:219], v[6:9], v[32:47]
	v_cvt_scalef32_pk_bf16_fp8 v6, v204, 1.0
	v_cvt_scalef32_pk_bf16_fp8 v7, v204, 1.0 op_sel:[1,0,0]
	v_cvt_scalef32_pk_bf16_fp8 v8, v205, 1.0
	v_cvt_scalef32_pk_bf16_fp8 v9, v205, 1.0 op_sel:[1,0,0]
	ds_read_b128 v[10:13], v0 offset:4640
	s_waitcnt lgkmcnt(2)
	v_mfma_f32_32x32x16_bf16 v[144:159], v[2:5], v[6:9], v[144:159]
	s_waitcnt lgkmcnt(0)
	v_mfma_f32_32x32x16_bf16 v[112:127], v[10:13], v[6:9], v[112:127]
	v_mfma_f32_32x32x16_bf16 v[128:143], v[208:211], v[6:9], v[128:143]
	v_mfma_f32_32x32x16_bf16 v[96:111], v[212:215], v[6:9], v[96:111]
	v_cvt_pk_f32_fp8_e32 v[6:7], v192
	v_cvt_pk_f32_fp8_sdwa v[8:9], v192 src0_sel:WORD_1
	v_cvt_pk_f32_fp8_sdwa v[192:193], v193 src0_sel:WORD_1
	v_cvt_pk_bf16_f32 v6, v6, v7
	v_cvt_pk_bf16_f32 v7, v8, v9
	v_cvt_pk_bf16_f32 v8, v14, v15
	v_cvt_pk_bf16_f32 v9, v192, v193
	s_nop 1
	v_mfma_f32_32x32x16_bf16 v[80:95], v[2:5], v[6:9], v[80:95]
	ds_read_b128 v[2:5], v0 offset:48
	v_mfma_f32_32x32x16_bf16 v[48:63], v[10:13], v[6:9], v[48:63]
	v_cvt_pk_f32_fp8_e32 v[10:11], v207
	v_cvt_pk_f32_fp8_sdwa v[12:13], v207 src0_sel:WORD_1
	v_mfma_f32_32x32x16_bf16 v[64:79], v[208:211], v[6:9], v[64:79]
	ds_read_b128 v[208:211], v0 offset:13872
	v_mfma_f32_32x32x16_bf16 v[32:47], v[212:215], v[6:9], v[32:47]
	v_cvt_pk_f32_fp8_e32 v[6:7], v206
	v_cvt_pk_f32_fp8_sdwa v[8:9], v206 src0_sel:WORD_1
	ds_read_b128 v[204:207], v0 offset:9264
	v_cvt_pk_bf16_f32 v6, v6, v7
	v_cvt_pk_bf16_f32 v7, v8, v9
	v_cvt_pk_bf16_f32 v8, v10, v11
	v_cvt_pk_bf16_f32 v9, v12, v13
	ds_read_b128 v[10:13], v0 offset:4656
	s_waitcnt lgkmcnt(3)
	v_mfma_f32_32x32x16_bf16 v[144:159], v[2:5], v[6:9], v[144:159]
	s_waitcnt lgkmcnt(0)
	v_mfma_f32_32x32x16_bf16 v[112:127], v[10:13], v[6:9], v[112:127]
	v_mfma_f32_32x32x16_bf16 v[128:143], v[204:207], v[6:9], v[128:143]
	v_mfma_f32_32x32x16_bf16 v[96:111], v[208:211], v[6:9], v[96:111]
	v_cvt_scalef32_pk_bf16_fp8 v6, v194, 1.0
	v_cvt_scalef32_pk_bf16_fp8 v7, v194, 1.0 op_sel:[1,0,0]
	v_cvt_scalef32_pk_bf16_fp8 v8, v195, 1.0
	v_cvt_scalef32_pk_bf16_fp8 v9, v195, 1.0 op_sel:[1,0,0]
	s_nop 1
	v_mfma_f32_32x32x16_bf16 v[80:95], v[2:5], v[6:9], v[80:95]
	v_mfma_f32_32x32x16_bf16 v[48:63], v[10:13], v[6:9], v[48:63]
	v_mfma_f32_32x32x16_bf16 v[64:79], v[204:207], v[6:9], v[64:79]
	v_mfma_f32_32x32x16_bf16 v[32:47], v[208:211], v[6:9], v[32:47]
.LBB0_1308:
	v_mov_b32_e32 v0, v241
	s_waitcnt vmcnt(5)
	global_load_dwordx4 v[192:195], v0, s[46:47] offset:16
	global_load_dwordx4 v[208:211], v0, s[46:47]
	v_mov_b32_e32 v0, v242
	global_load_dwordx4 v[6:9], v0, s[46:47] offset:16
	global_load_dwordx4 v[204:207], v0, s[46:47]
	v_add_u32_e32 v0, s90, v246
	v_cvt_scalef32_pk_bf16_fp8 v2, v196, 1.0
	v_cvt_scalef32_pk_bf16_fp8 v3, v196, 1.0 op_sel:[1,0,0]
	v_cvt_scalef32_pk_bf16_fp8 v4, v197, 1.0
	v_cvt_scalef32_pk_bf16_fp8 v5, v197, 1.0 op_sel:[1,0,0]
	ds_read_b128 v[10:13], v0
	v_cvt_pk_f32_fp8_sdwa v[14:15], v199 src0_sel:WORD_1
	s_waitcnt lgkmcnt(0)
	v_mfma_f32_32x32x16_bf16 v[16:31], v[10:13], v[2:5], v[16:31]
	v_cvt_pk_f32_fp8_e32 v[12:13], v199
	s_add_i32 s2, s26, 1
	v_cvt_scalef32_pk_bf16_fp8 v10, v198, 1.0
	v_mov_b32_e32 v2, v243
	v_cvt_scalef32_pk_bf16_fp8 v11, v198, 1.0 op_sel:[1,0,0]
	global_load_dwordx4 v[2:5], v2, s[46:47]
	ds_read_b128 v[196:199], v0 offset:16
	ds_read_b128 v[212:215], v0 offset:32
	v_cvt_pk_bf16_f32 v12, v12, v13
	v_cvt_pk_bf16_f32 v13, v14, v15
	s_waitcnt vmcnt(9)
	v_cvt_pk_f32_fp8_e32 v[14:15], v201
	s_cmp_lg_u32 s26, 2
	s_waitcnt lgkmcnt(1)
	v_mfma_f32_32x32x16_bf16 v[16:31], v[196:199], v[10:13], v[16:31]
	v_cvt_pk_f32_fp8_e32 v[10:11], v200
	v_cvt_pk_f32_fp8_sdwa v[12:13], v200 src0_sel:WORD_1
	v_cvt_pk_f32_fp8_sdwa v[196:197], v201 src0_sel:WORD_1
	v_cvt_pk_bf16_f32 v10, v10, v11
	v_cvt_pk_bf16_f32 v11, v12, v13
	v_cvt_pk_bf16_f32 v12, v14, v15
	v_cvt_pk_bf16_f32 v13, v196, v197
	s_cselect_b32 s2, s2, 0
	s_mul_i32 s25, s2, 0x4800
	s_waitcnt lgkmcnt(0)
	v_mfma_f32_32x32x16_bf16 v[16:31], v[212:215], v[10:13], v[16:31]
	v_cvt_pk_f32_fp8_sdwa v[12:13], v202 src0_sel:WORD_1
	v_cvt_pk_f32_fp8_e32 v[14:15], v203
	v_cvt_scalef32_pk_bf16_fp8 v199, v203, 1.0 op_sel:[1,0,0]
	v_cvt_scalef32_pk_bf16_fp8 v196, v202, 1.0
	v_mov_b32_e32 v10, v243
	ds_read_b128 v[200:203], v0 offset:48
	v_add_u32_e32 v0, s25, v244
	s_add_i32 s25, s39, 4
	s_cmp_lt_u32 s39, 60
	s_cselect_b32 s25, s25, 0
	s_lshr_b32 s26, s25, 4
	s_add_i32 s26, s26, s66
	s_and_b32 s26, s26, 3
	s_add_i32 s26, s26, s27
	s_lshl_b32 s25, s25, 16
	s_lshl_b32 s26, s26, 8
	s_and_b32 s25, s25, 0xe0000
	v_cvt_pk_bf16_f32 v198, v14, v15
	s_waitcnt vmcnt(11)
	v_cvt_pk_bf16_f32 v14, v176, v180
	s_waitcnt vmcnt(9)
	v_cvt_pk_bf16_f32 v15, v184, v188
	s_or_b32 s25, s26, s25
	v_cvt_pk_bf16_f32 v197, v12, v13
	global_load_dwordx4 v[10:13], v10, s[46:47] offset:16
	s_waitcnt lgkmcnt(0)
	s_barrier
	ds_write2_b32 v0, v14, v15 offset1:8
	v_cvt_pk_bf16_f32 v14, v177, v181
	v_cvt_pk_bf16_f32 v15, v185, v189
	v_add_u32_e32 v176, 0x400, v0
	s_add_u32 s46, s67, s25
	ds_write2_b32 v176, v14, v15 offset0:32 offset1:40
	v_cvt_pk_bf16_f32 v14, v178, v182
	v_cvt_pk_bf16_f32 v15, v186, v190
	v_add_u32_e32 v176, 0x800, v0
	s_addc_u32 s47, s38, 0
	ds_write2_b32 v176, v14, v15 offset0:64 offset1:72
	v_cvt_pk_bf16_f32 v14, v179, v183
	v_cvt_pk_bf16_f32 v15, v187, v191
	v_add_u32_e32 v0, 0xc00, v0
	s_add_u32 s90, s46, 0x4000
	ds_write2_b32 v0, v14, v15 offset0:96 offset1:104
	s_addc_u32 s91, s47, 0
	v_mov_b32_e32 v0, v238
	global_load_dwordx4 v[176:179], v0, s[46:47] nt
	global_load_dwordx4 v[180:183], v0, s[46:47] offset:1024 nt
	global_load_dwordx4 v[184:187], v0, s[90:91] nt
	global_load_dwordx4 v[188:191], v0, s[90:91] offset:1024 nt
	v_mfma_f32_32x32x16_bf16 v[16:31], v[200:203], v[196:199], v[16:31]
	s_cmp_gt_u32 s39, 61
	s_cselect_b64 s[46:47], -1, 0
	s_and_b32 s25, s49, 0x380
	s_cmp_lt_u32 s39, 62
	s_cselect_b32 s25, s25, 0
	s_add_u32 s90, s25, s54
	s_addc_u32 s91, 0, s55
	s_and_b64 vcc, exec, s[42:43]
	s_cbranch_vccnz .LBB0_1310
	s_waitcnt vmcnt(8)
	v_add_u32_e32 v0, s56, v240
	ds_read_b128 v[196:199], v0
	v_cvt_scalef32_pk_bf16_fp8 v201, v208, 1.0 op_sel:[1,0,0]
	v_cvt_scalef32_pk_bf16_fp8 v202, v209, 1.0
	ds_read_b128 v[212:215], v0 offset:4608
	ds_read_b128 v[216:219], v0 offset:9216
	ds_read_b128 v[248:251], v0 offset:13824
	v_cvt_pk_f32_fp8_e32 v[14:15], v208
	v_cvt_pk_f32_fp8_sdwa v[208:209], v209 src0_sel:WORD_1
	v_cvt_pk_bf16_f32 v200, v14, v15
	v_cvt_pk_bf16_f32 v203, v208, v209
	s_waitcnt vmcnt(6)
	v_cvt_pk_f32_fp8_e32 v[14:15], v204
	v_cvt_pk_f32_fp8_e32 v[208:209], v205
	s_waitcnt lgkmcnt(3)
	v_mfma_f32_32x32x16_bf16 v[144:159], v[196:199], v[200:203], v[144:159]
	s_waitcnt lgkmcnt(2)
	v_mfma_f32_32x32x16_bf16 v[112:127], v[212:215], v[200:203], v[112:127]
	s_waitcnt lgkmcnt(1)
	v_mfma_f32_32x32x16_bf16 v[128:143], v[216:219], v[200:203], v[128:143]
	s_waitcnt lgkmcnt(0)
	v_mfma_f32_32x32x16_bf16 v[96:111], v[248:251], v[200:203], v[96:111]
	v_cvt_pk_f32_fp8_sdwa v[202:203], v204 src0_sel:WORD_1
	v_cvt_pk_f32_fp8_sdwa v[204:205], v205 src0_sel:WORD_1
	v_cvt_pk_bf16_f32 v200, v14, v15
	v_cvt_pk_bf16_f32 v201, v202, v203
	v_cvt_pk_bf16_f32 v202, v208, v209
	v_cvt_pk_bf16_f32 v203, v204, v205
	v_cvt_pk_f32_fp8_e32 v[204:205], v211
	s_nop 0
	v_mfma_f32_32x32x16_bf16 v[80:95], v[196:199], v[200:203], v[80:95]
	ds_read_b128 v[196:199], v0 offset:16
	v_mfma_f32_32x32x16_bf16 v[48:63], v[212:215], v[200:203], v[48:63]
	ds_read_b128 v[212:215], v0 offset:9232
	v_mfma_f32_32x32x16_bf16 v[64:79], v[216:219], v[200:203], v[64:79]
	ds_read_b128 v[216:219], v0 offset:13840
	v_mfma_f32_32x32x16_bf16 v[32:47], v[248:251], v[200:203], v[32:47]
	v_cvt_scalef32_pk_bf16_fp8 v200, v210, 1.0
	v_cvt_pk_f32_fp8_e32 v[14:15], v206
	v_cvt_scalef32_pk_bf16_fp8 v201, v210, 1.0 op_sel:[1,0,0]
	v_cvt_scalef32_pk_bf16_fp8 v203, v211, 1.0 op_sel:[1,0,0]
	ds_read_b128 v[208:211], v0 offset:4624
	v_cvt_pk_bf16_f32 v202, v204, v205
	v_cvt_pk_f32_fp8_e32 v[204:205], v207
	s_waitcnt lgkmcnt(3)
	v_mfma_f32_32x32x16_bf16 v[144:159], v[196:199], v[200:203], v[144:159]
	s_waitcnt lgkmcnt(0)
	v_mfma_f32_32x32x16_bf16 v[112:127], v[208:211], v[200:203], v[112:127]
	v_mfma_f32_32x32x16_bf16 v[128:143], v[212:215], v[200:203], v[128:143]
	v_mfma_f32_32x32x16_bf16 v[96:111], v[216:219], v[200:203], v[96:111]
	v_cvt_pk_f32_fp8_sdwa v[202:203], v206 src0_sel:WORD_1
	v_cvt_pk_f32_fp8_sdwa v[206:207], v207 src0_sel:WORD_1
	v_cvt_pk_bf16_f32 v200, v14, v15
	v_cvt_pk_f32_fp8_e32 v[14:15], v192
	v_cvt_pk_bf16_f32 v201, v202, v203
	v_cvt_pk_bf16_f32 v202, v204, v205
	v_cvt_pk_bf16_f32 v203, v206, v207
	v_cvt_pk_f32_fp8_e32 v[204:205], v193
	s_nop 0
	v_mfma_f32_32x32x16_bf16 v[80:95], v[196:199], v[200:203], v[80:95]
	ds_read_b128 v[196:199], v0 offset:32
	v_mfma_f32_32x32x16_bf16 v[48:63], v[208:211], v[200:203], v[48:63]
	ds_read_b128 v[208:211], v0 offset:9248
	v_mfma_f32_32x32x16_bf16 v[64:79], v[212:215], v[200:203], v[64:79]
	ds_read_b128 v[212:215], v0 offset:13856
	v_mfma_f32_32x32x16_bf16 v[32:47], v[216:219], v[200:203], v[32:47]
	v_cvt_pk_f32_fp8_sdwa v[202:203], v192 src0_sel:WORD_1
	v_cvt_pk_f32_fp8_sdwa v[192:193], v193 src0_sel:WORD_1
	v_cvt_pk_bf16_f32 v200, v14, v15
	v_cvt_pk_f32_fp8_e32 v[14:15], v6
	v_cvt_pk_bf16_f32 v201, v202, v203
	v_cvt_pk_bf16_f32 v202, v204, v205
	ds_read_b128 v[204:207], v0 offset:4640
	v_cvt_pk_bf16_f32 v203, v192, v193
	v_cvt_pk_f32_fp8_sdwa v[192:193], v6 src0_sel:WORD_1
	s_waitcnt lgkmcnt(3)
	v_mfma_f32_32x32x16_bf16 v[144:159], v[196:199], v[200:203], v[144:159]
	s_waitcnt lgkmcnt(0)
	v_mfma_f32_32x32x16_bf16 v[112:127], v[204:207], v[200:203], v[112:127]
	v_mfma_f32_32x32x16_bf16 v[128:143], v[208:211], v[200:203], v[128:143]
	v_mfma_f32_32x32x16_bf16 v[96:111], v[212:215], v[200:203], v[96:111]
	v_cvt_pk_f32_fp8_e32 v[202:203], v7
	v_cvt_pk_f32_fp8_sdwa v[6:7], v7 src0_sel:WORD_1
	v_cvt_pk_bf16_f32 v200, v14, v15
	v_cvt_pk_bf16_f32 v201, v192, v193
	v_cvt_pk_bf16_f32 v202, v202, v203
	v_cvt_pk_bf16_f32 v203, v6, v7
	s_nop 1
	v_mfma_f32_32x32x16_bf16 v[80:95], v[196:199], v[200:203], v[80:95]
	ds_read_b128 v[196:199], v0 offset:48
	v_cvt_scalef32_pk_bf16_fp8 v192, v194, 1.0
	v_cvt_scalef32_pk_bf16_fp8 v193, v194, 1.0 op_sel:[1,0,0]
	v_cvt_scalef32_pk_bf16_fp8 v6, v8, 1.0
	v_mfma_f32_32x32x16_bf16 v[48:63], v[204:207], v[200:203], v[48:63]
	ds_read_b128 v[204:207], v0 offset:9264
	v_cvt_scalef32_pk_bf16_fp8 v7, v8, 1.0 op_sel:[1,0,0]
	v_mfma_f32_32x32x16_bf16 v[64:79], v[208:211], v[200:203], v[64:79]
	ds_read_b128 v[208:211], v0 offset:13872
	v_mfma_f32_32x32x16_bf16 v[32:47], v[212:215], v[200:203], v[32:47]
	v_cvt_scalef32_pk_bf16_fp8 v194, v195, 1.0
	v_cvt_scalef32_pk_bf16_fp8 v195, v195, 1.0 op_sel:[1,0,0]
	ds_read_b128 v[200:203], v0 offset:4656
	s_waitcnt lgkmcnt(3)
	v_mfma_f32_32x32x16_bf16 v[144:159], v[196:199], v[192:195], v[144:159]
	s_waitcnt lgkmcnt(0)
	v_mfma_f32_32x32x16_bf16 v[112:127], v[200:203], v[192:195], v[112:127]
	v_mfma_f32_32x32x16_bf16 v[128:143], v[204:207], v[192:195], v[128:143]
	v_mfma_f32_32x32x16_bf16 v[96:111], v[208:211], v[192:195], v[96:111]
	v_cvt_scalef32_pk_bf16_fp8 v8, v9, 1.0
	v_cvt_scalef32_pk_bf16_fp8 v9, v9, 1.0 op_sel:[1,0,0]
	s_nop 1
	v_mfma_f32_32x32x16_bf16 v[80:95], v[196:199], v[6:9], v[80:95]
	v_mfma_f32_32x32x16_bf16 v[48:63], v[200:203], v[6:9], v[48:63]
	v_mfma_f32_32x32x16_bf16 v[64:79], v[204:207], v[6:9], v[64:79]
	v_mfma_f32_32x32x16_bf16 v[32:47], v[208:211], v[6:9], v[32:47]
.LBB0_1310:
	v_mov_b32_e32 v0, v241
	global_load_dwordx4 v[204:207], v0, s[90:91] offset:16
	global_load_dwordx4 v[212:215], v0, s[90:91]
	v_mov_b32_e32 v0, v242
	s_add_i32 s25, s33, s56
	global_load_dwordx4 v[192:195], v0, s[90:91] offset:16
	global_load_dwordx4 v[208:211], v0, s[90:91]
	v_add_u32_e32 v0, s25, v240
	ds_read_b128 v[196:199], v0
	s_waitcnt vmcnt(9)
	v_cvt_pk_f32_fp8_e32 v[6:7], v2
	v_cvt_pk_f32_fp8_sdwa v[8:9], v2 src0_sel:WORD_1
	v_cvt_pk_f32_fp8_e32 v[14:15], v3
	v_cvt_pk_f32_fp8_sdwa v[2:3], v3 src0_sel:WORD_1
	v_cvt_pk_bf16_f32 v6, v6, v7
	v_cvt_pk_bf16_f32 v7, v8, v9
	v_cvt_pk_bf16_f32 v8, v14, v15
	v_cvt_pk_bf16_f32 v9, v2, v3
	s_waitcnt lgkmcnt(0)
	s_nop 0
	v_mfma_f32_32x32x16_bf16 v[16:31], v[196:199], v[6:9], v[16:31]
	v_cvt_pk_f32_fp8_e32 v[8:9], v5
	v_cvt_scalef32_pk_bf16_fp8 v2, v4, 1.0
	v_cvt_scalef32_pk_bf16_fp8 v5, v5, 1.0 op_sel:[1,0,0]
	v_cvt_scalef32_pk_bf16_fp8 v3, v4, 1.0 op_sel:[1,0,0]
	v_mov_b32_e32 v6, v243
	v_cvt_pk_bf16_f32 v4, v8, v9
	global_load_dwordx4 v[196:199], v6, s[90:91]
	ds_read_b128 v[6:9], v0 offset:16
	ds_read_b128 v[200:203], v0 offset:32
	s_waitcnt lgkmcnt(1)
	v_mfma_f32_32x32x16_bf16 v[16:31], v[6:9], v[2:5], v[16:31]
	s_waitcnt vmcnt(9)
	v_cvt_scalef32_pk_bf16_fp8 v2, v10, 1.0
	v_cvt_scalef32_pk_bf16_fp8 v3, v10, 1.0 op_sel:[1,0,0]
	v_cvt_scalef32_pk_bf16_fp8 v4, v11, 1.0
	v_cvt_scalef32_pk_bf16_fp8 v5, v11, 1.0 op_sel:[1,0,0]
	s_waitcnt lgkmcnt(0)
	s_nop 0
	v_mfma_f32_32x32x16_bf16 v[16:31], v[200:203], v[2:5], v[16:31]
	s_and_b32 s26, s39, 14
	s_cmp_lg_u32 s26, 14
	v_cvt_scalef32_pk_bf16_fp8 v2, v12, 1.0
	v_cvt_scalef32_pk_bf16_fp8 v3, v12, 1.0 op_sel:[1,0,0]
	v_cvt_scalef32_pk_bf16_fp8 v4, v13, 1.0
	v_mov_b32_e32 v6, v243
	global_load_dwordx4 v[200:203], v6, s[90:91] offset:16
	v_cvt_scalef32_pk_bf16_fp8 v5, v13, 1.0 op_sel:[1,0,0]
	ds_read_b128 v[6:9], v0 offset:48
	s_waitcnt lgkmcnt(0)
	v_mfma_f32_32x32x16_bf16 v[16:31], v[6:9], v[2:5], v[16:31]
	s_cbranch_scc1 .LBB0_1305
	s_lshr_b32 s25, s39, 4
	s_add_i32 s25, s25, s66
	v_mbcnt_lo_u32_b32 v248, -1, 0
	v_mbcnt_hi_u32_b32 v248, -1, v248
	s_and_b32 s56, s25, 3
	v_ashrrev_i32_e32 v0, 5, v248
	v_lshlrev_b32_e32 v218, 4, v0
	s_add_i32 s56, s56, s27
	v_and_b32_e32 v247, 31, v248
	s_and_b64 vcc, exec, s[42:43]
	v_ashrrev_i32_e32 v219, 31, v218
	s_cbranch_vccnz .LBB0_1315
	v_lshl_add_u32 v6, v247, 2, s87
	ds_read_b32 v0, v6 offset:55296
	s_lshl_b32 s25, s56, 6
	s_add_u32 s42, s58, s25
	s_addc_u32 s43, s59, 0
	v_lshl_add_u64 v[2:3], s[42:43], 0, v[218:219]
	s_waitcnt lgkmcnt(0)
	v_lshlrev_b64 v[4:5], 8, v[0:1]
	v_mul_f32_e32 v0, 0xbfb8aa3b, v144
	v_exp_f32_e32 v0, v0
	v_lshl_add_u64 v[4:5], v[2:3], 0, v[4:5]
	v_add_f32_e32 v0, 1.0, v0
	v_div_scale_f32 v7, s[42:43], v0, v0, v144
	v_rcp_f32_e32 v8, v7
	s_nop 0
	v_fma_f32 v9, -v7, v8, 1.0
	v_fmac_f32_e32 v8, v9, v8
	v_div_scale_f32 v9, vcc, v144, v0, v144
	v_mul_f32_e32 v10, v9, v8
	v_fma_f32 v11, -v7, v10, v9
	v_fmac_f32_e32 v10, v11, v8
	v_fma_f32 v7, -v7, v10, v9
	v_div_fmas_f32 v7, v7, v8, v10
	v_div_fixup_f32 v0, v7, v0, v144
	v_mul_f32_e32 v7, 0xbfb8aa3b, v148
	v_exp_f32_e32 v7, v7
	v_mul_f32_e32 v0, v128, v0
	v_add_f32_e32 v7, 1.0, v7
	v_div_scale_f32 v8, s[42:43], v7, v7, v148
	v_rcp_f32_e32 v9, v8
	s_nop 0
	v_fma_f32 v10, -v8, v9, 1.0
	v_fmac_f32_e32 v9, v10, v9
	v_div_scale_f32 v10, vcc, v148, v7, v148
	v_mul_f32_e32 v11, v10, v9
	v_fma_f32 v12, -v8, v11, v10
	v_fmac_f32_e32 v11, v12, v9
	v_fma_f32 v8, -v8, v11, v10
	v_div_fmas_f32 v8, v8, v9, v11
	v_div_fixup_f32 v7, v8, v7, v148
	v_mul_f32_e32 v8, 0xbfb8aa3b, v152
	v_exp_f32_e32 v8, v8
	v_mul_f32_e32 v7, v132, v7
	v_add_f32_e32 v8, 1.0, v8
	v_div_scale_f32 v9, s[42:43], v8, v8, v152
	v_rcp_f32_e32 v10, v9
	s_nop 0
	v_fma_f32 v11, -v9, v10, 1.0
	v_fmac_f32_e32 v10, v11, v10
	v_div_scale_f32 v11, vcc, v152, v8, v152
	v_mul_f32_e32 v12, v11, v10
	v_fma_f32 v13, -v9, v12, v11
	v_fmac_f32_e32 v12, v13, v10
	v_fma_f32 v9, -v9, v12, v11
	v_div_fmas_f32 v9, v9, v10, v12
	v_div_fixup_f32 v8, v9, v8, v152
	v_mul_f32_e32 v9, 0xbfb8aa3b, v156
	v_exp_f32_e32 v9, v9
	v_mul_f32_e32 v8, v136, v8
	v_add_f32_e32 v9, 1.0, v9
	v_div_scale_f32 v10, s[42:43], v9, v9, v156
	v_rcp_f32_e32 v11, v10
	s_nop 0
	v_fma_f32 v12, -v10, v11, 1.0
	v_fmac_f32_e32 v11, v12, v11
	v_div_scale_f32 v12, vcc, v156, v9, v156
	v_mul_f32_e32 v13, v12, v11
	v_fma_f32 v14, -v10, v13, v12
	v_fmac_f32_e32 v13, v14, v11
	v_fma_f32 v10, -v10, v13, v12
	v_div_fmas_f32 v10, v10, v11, v13
	v_div_fixup_f32 v9, v10, v9, v156
	v_mul_f32_e32 v10, 0xbfb8aa3b, v145
	v_exp_f32_e32 v10, v10
	v_mul_f32_e32 v9, v140, v9
	v_add_f32_e32 v10, 1.0, v10
	v_div_scale_f32 v11, s[42:43], v10, v10, v145
	v_rcp_f32_e32 v12, v11
	s_nop 0
	v_fma_f32 v13, -v11, v12, 1.0
	v_fmac_f32_e32 v12, v13, v12
	v_div_scale_f32 v13, vcc, v145, v10, v145
	v_mul_f32_e32 v14, v13, v12
	v_fma_f32 v15, -v11, v14, v13
	v_fmac_f32_e32 v14, v15, v12
	v_fma_f32 v11, -v11, v14, v13
	v_div_fmas_f32 v11, v11, v12, v14
	v_div_fixup_f32 v10, v11, v10, v145
	v_mul_f32_e32 v11, 0xbfb8aa3b, v149
	v_exp_f32_e32 v11, v11
	v_mul_f32_e32 v10, v129, v10
	v_add_f32_e32 v11, 1.0, v11
	v_div_scale_f32 v12, s[42:43], v11, v11, v149
	v_rcp_f32_e32 v13, v12
	s_nop 0
	v_fma_f32 v14, -v12, v13, 1.0
	v_fmac_f32_e32 v13, v14, v13
	v_div_scale_f32 v14, vcc, v149, v11, v149
	v_mul_f32_e32 v15, v14, v13
	v_fma_f32 v128, -v12, v15, v14
	v_fmac_f32_e32 v15, v128, v13
	v_fma_f32 v12, -v12, v15, v14
	v_div_fmas_f32 v12, v12, v13, v15
	v_div_fixup_f32 v11, v12, v11, v149
	v_mul_f32_e32 v12, 0xbfb8aa3b, v153
	v_exp_f32_e32 v12, v12
	v_mul_f32_e32 v11, v133, v11
	v_add_f32_e32 v12, 1.0, v12
	v_div_scale_f32 v13, s[42:43], v12, v12, v153
	v_rcp_f32_e32 v14, v13
	s_nop 0
	v_fma_f32 v15, -v13, v14, 1.0
	v_fmac_f32_e32 v14, v15, v14
	v_div_scale_f32 v15, vcc, v153, v12, v153
	v_mul_f32_e32 v128, v15, v14
	v_fma_f32 v129, -v13, v128, v15
	v_fmac_f32_e32 v128, v129, v14
	v_fma_f32 v13, -v13, v128, v15
	v_div_fmas_f32 v13, v13, v14, v128
	v_div_fixup_f32 v12, v13, v12, v153
	v_mul_f32_e32 v13, 0xbfb8aa3b, v157
	v_exp_f32_e32 v13, v13
	v_mul_f32_e32 v12, v137, v12
	v_add_f32_e32 v13, 1.0, v13
	v_div_scale_f32 v14, s[42:43], v13, v13, v157
	v_rcp_f32_e32 v15, v14
	s_nop 0
	v_fma_f32 v128, -v14, v15, 1.0
	v_fmac_f32_e32 v15, v128, v15
	v_div_scale_f32 v128, vcc, v157, v13, v157
	v_mul_f32_e32 v129, v128, v15
	v_fma_f32 v132, -v14, v129, v128
	v_fmac_f32_e32 v129, v132, v15
	v_fma_f32 v14, -v14, v129, v128
	v_div_fmas_f32 v14, v14, v15, v129
	v_div_fixup_f32 v13, v14, v13, v157
	v_mul_f32_e32 v14, 0xbfb8aa3b, v146
	v_exp_f32_e32 v14, v14
	v_mul_f32_e32 v13, v141, v13
	v_add_f32_e32 v14, 1.0, v14
	v_div_scale_f32 v15, s[42:43], v14, v14, v146
	v_rcp_f32_e32 v128, v15
	s_nop 0
	v_fma_f32 v129, -v15, v128, 1.0
	v_fmac_f32_e32 v128, v129, v128
	v_div_scale_f32 v129, vcc, v146, v14, v146
	v_mul_f32_e32 v132, v129, v128
	v_fma_f32 v133, -v15, v132, v129
	v_fmac_f32_e32 v132, v133, v128
	v_fma_f32 v15, -v15, v132, v129
	v_div_fmas_f32 v15, v15, v128, v132
	v_div_fixup_f32 v14, v15, v14, v146
	v_mul_f32_e32 v15, 0xbfb8aa3b, v150
	v_exp_f32_e32 v15, v15
	v_mul_f32_e32 v14, v130, v14
	v_add_f32_e32 v15, 1.0, v15
	v_div_scale_f32 v128, s[42:43], v15, v15, v150
	v_rcp_f32_e32 v129, v128
	s_nop 0
	v_fma_f32 v130, -v128, v129, 1.0
	v_fmac_f32_e32 v129, v130, v129
	v_div_scale_f32 v130, vcc, v150, v15, v150
	v_mul_f32_e32 v132, v130, v129
	v_fma_f32 v133, -v128, v132, v130
	v_fmac_f32_e32 v132, v133, v129
	v_fma_f32 v128, -v128, v132, v130
	v_div_fmas_f32 v128, v128, v129, v132
	v_div_fixup_f32 v15, v128, v15, v150
	v_mul_f32_e32 v128, 0xbfb8aa3b, v154
	v_exp_f32_e32 v128, v128
	v_mul_f32_e32 v15, v134, v15
	v_add_f32_e32 v128, 1.0, v128
	v_div_scale_f32 v129, s[42:43], v128, v128, v154
	v_rcp_f32_e32 v130, v129
	s_nop 0
	v_fma_f32 v132, -v129, v130, 1.0
	v_fmac_f32_e32 v130, v132, v130
	v_div_scale_f32 v132, vcc, v154, v128, v154
	v_mul_f32_e32 v133, v132, v130
	v_fma_f32 v134, -v129, v133, v132
	v_fmac_f32_e32 v133, v134, v130
	v_fma_f32 v129, -v129, v133, v132
	v_div_fmas_f32 v129, v129, v130, v133
	v_div_fixup_f32 v128, v129, v128, v154
	v_mul_f32_e32 v132, v138, v128
	v_mul_f32_e32 v128, 0xbfb8aa3b, v158
	v_exp_f32_e32 v128, v128
	s_nop 0
	v_add_f32_e32 v128, 1.0, v128
	v_div_scale_f32 v129, s[42:43], v128, v128, v158
	v_rcp_f32_e32 v130, v129
	s_nop 0
	v_fma_f32 v133, -v129, v130, 1.0
	v_fmac_f32_e32 v130, v133, v130
	v_div_scale_f32 v133, vcc, v158, v128, v158
	v_mul_f32_e32 v134, v133, v130
	v_fma_f32 v136, -v129, v134, v133
	v_fmac_f32_e32 v134, v136, v130
	v_fma_f32 v129, -v129, v134, v133
	v_div_fmas_f32 v129, v129, v130, v134
	v_div_fixup_f32 v128, v129, v128, v158
	v_mul_f32_e32 v133, v142, v128
	v_mul_f32_e32 v128, 0xbfb8aa3b, v147
	v_exp_f32_e32 v128, v128
	s_nop 0
	v_add_f32_e32 v128, 1.0, v128
	v_div_scale_f32 v129, s[42:43], v128, v128, v147
	v_rcp_f32_e32 v130, v129
	s_nop 0
	v_fma_f32 v134, -v129, v130, 1.0
	v_fmac_f32_e32 v130, v134, v130
	v_div_scale_f32 v134, vcc, v147, v128, v147
	v_mul_f32_e32 v136, v134, v130
	v_fma_f32 v137, -v129, v136, v134
	v_fmac_f32_e32 v136, v137, v130
	v_fma_f32 v129, -v129, v136, v134
	v_div_fmas_f32 v129, v129, v130, v136
	v_div_fixup_f32 v128, v129, v128, v147
	v_mul_f32_e32 v134, v131, v128
	v_mul_f32_e32 v128, 0xbfb8aa3b, v151
	v_exp_f32_e32 v128, v128
	s_nop 0
	v_add_f32_e32 v128, 1.0, v128
	v_div_scale_f32 v129, s[42:43], v128, v128, v151
	v_rcp_f32_e32 v130, v129
	s_nop 0
	v_fma_f32 v131, -v129, v130, 1.0
	v_fmac_f32_e32 v130, v131, v130
	v_div_scale_f32 v131, vcc, v151, v128, v151
	v_mul_f32_e32 v136, v131, v130
	v_fma_f32 v137, -v129, v136, v131
	v_fmac_f32_e32 v136, v137, v130
	v_fma_f32 v129, -v129, v136, v131
	v_div_fmas_f32 v129, v129, v130, v136
	v_div_fixup_f32 v128, v129, v128, v151
	v_mul_f32_e32 v135, v135, v128
	v_mul_f32_e32 v128, 0xbfb8aa3b, v155
	v_exp_f32_e32 v128, v128
	s_nop 0
	v_add_f32_e32 v128, 1.0, v128
	v_div_scale_f32 v129, s[42:43], v128, v128, v155
	v_rcp_f32_e32 v130, v129
	s_nop 0
	v_fma_f32 v131, -v129, v130, 1.0
	v_fmac_f32_e32 v130, v131, v130
	v_div_scale_f32 v131, vcc, v155, v128, v155
	v_mul_f32_e32 v136, v131, v130
	v_fma_f32 v137, -v129, v136, v131
	v_fmac_f32_e32 v136, v137, v130
	v_fma_f32 v129, -v129, v136, v131
	v_div_fmas_f32 v129, v129, v130, v136
	v_div_fixup_f32 v128, v129, v128, v155
	v_mul_f32_e32 v136, v139, v128
	v_mul_f32_e32 v128, 0xbfb8aa3b, v159
	v_exp_f32_e32 v128, v128
	s_nop 0
	v_add_f32_e32 v128, 1.0, v128
	v_div_scale_f32 v129, s[42:43], v128, v128, v159
	v_rcp_f32_e32 v130, v129
	s_nop 0
	v_fma_f32 v131, -v129, v130, 1.0
	v_fmac_f32_e32 v130, v131, v130
	v_div_scale_f32 v131, vcc, v159, v128, v159
	v_mul_f32_e32 v137, v131, v130
	v_fma_f32 v138, -v129, v137, v131
	v_fmac_f32_e32 v137, v138, v130
	v_fma_f32 v129, -v129, v137, v131
	v_div_fmas_f32 v129, v129, v130, v137
	v_div_fixup_f32 v128, v129, v128, v159
	v_mul_f32_e32 v137, v143, v128
	v_mov_b32_e32 v128, v1
	v_cvt_pk_fp8_f32 v128, v0, v7
	v_mul_f32_e32 v0, 0xbfb8aa3b, v112
	v_exp_f32_e32 v0, v0
	v_mov_b32_e32 v129, v1
	v_cvt_pk_fp8_f32 v128, v8, v9 op_sel:[0,0,1]
	v_cvt_pk_fp8_f32 v129, v10, v11
	v_add_f32_e32 v0, 1.0, v0
	v_div_scale_f32 v7, s[42:43], v0, v0, v112
	v_rcp_f32_e32 v8, v7
	v_cvt_pk_fp8_f32 v129, v12, v13 op_sel:[0,0,1]
	v_mov_b32_e32 v130, v1
	v_cvt_pk_fp8_f32 v130, v14, v15
	v_fma_f32 v9, -v7, v8, 1.0
	v_fmac_f32_e32 v8, v9, v8
	v_div_scale_f32 v9, vcc, v112, v0, v112
	v_mul_f32_e32 v10, v9, v8
	v_fma_f32 v11, -v7, v10, v9
	v_fmac_f32_e32 v10, v11, v8
	v_fma_f32 v7, -v7, v10, v9
	v_div_fmas_f32 v7, v7, v8, v10
	v_div_fixup_f32 v0, v7, v0, v112
	v_mul_f32_e32 v7, 0xbfb8aa3b, v116
	v_exp_f32_e32 v7, v7
	v_mul_f32_e32 v0, v96, v0
	v_mov_b32_e32 v131, v1
	v_cvt_pk_fp8_f32 v131, v134, v135
	v_add_f32_e32 v7, 1.0, v7
	v_div_scale_f32 v8, s[42:43], v7, v7, v116
	v_rcp_f32_e32 v9, v8
	v_cvt_pk_fp8_f32 v130, v132, v133 op_sel:[0,0,1]
	v_cvt_pk_fp8_f32 v131, v136, v137 op_sel:[0,0,1]
	v_fma_f32 v10, -v8, v9, 1.0
	v_fmac_f32_e32 v9, v10, v9
	v_div_scale_f32 v10, vcc, v116, v7, v116
	v_mul_f32_e32 v11, v10, v9
	v_fma_f32 v12, -v8, v11, v10
	v_fmac_f32_e32 v11, v12, v9
	v_fma_f32 v8, -v8, v11, v10
	v_div_fmas_f32 v8, v8, v9, v11
	v_div_fixup_f32 v7, v8, v7, v116
	v_mul_f32_e32 v8, 0xbfb8aa3b, v120
	v_exp_f32_e32 v8, v8
	v_mul_f32_e32 v7, v100, v7
	global_store_dwordx4 v[4:5], v[128:131], off
	v_add_f32_e32 v8, 1.0, v8
	v_div_scale_f32 v9, s[42:43], v8, v8, v120
	v_rcp_f32_e32 v10, v9
	s_nop 0
	v_fma_f32 v11, -v9, v10, 1.0
	v_fmac_f32_e32 v10, v11, v10
	v_div_scale_f32 v11, vcc, v120, v8, v120
	v_mul_f32_e32 v12, v11, v10
	v_fma_f32 v13, -v9, v12, v11
	v_fmac_f32_e32 v12, v13, v10
	v_fma_f32 v9, -v9, v12, v11
	v_div_fmas_f32 v9, v9, v10, v12
	v_div_fixup_f32 v8, v9, v8, v120
	v_mul_f32_e32 v9, 0xbfb8aa3b, v124
	v_exp_f32_e32 v9, v9
	v_mul_f32_e32 v8, v104, v8
	v_add_f32_e32 v9, 1.0, v9
	v_div_scale_f32 v10, s[42:43], v9, v9, v124
	v_rcp_f32_e32 v11, v10
	s_nop 0
	v_fma_f32 v12, -v10, v11, 1.0
	v_fmac_f32_e32 v11, v12, v11
	v_div_scale_f32 v12, vcc, v124, v9, v124
	v_mul_f32_e32 v13, v12, v11
	v_fma_f32 v14, -v10, v13, v12
	v_fmac_f32_e32 v13, v14, v11
	v_fma_f32 v10, -v10, v13, v12
	v_div_fmas_f32 v10, v10, v11, v13
	v_div_fixup_f32 v9, v10, v9, v124
	v_mul_f32_e32 v10, 0xbfb8aa3b, v113
	v_exp_f32_e32 v10, v10
	v_mul_f32_e32 v9, v108, v9
	v_add_f32_e32 v10, 1.0, v10
	v_div_scale_f32 v11, s[42:43], v10, v10, v113
	v_rcp_f32_e32 v12, v11
	s_nop 0
	v_fma_f32 v13, -v11, v12, 1.0
	v_fmac_f32_e32 v12, v13, v12
	v_div_scale_f32 v13, vcc, v113, v10, v113
	v_mul_f32_e32 v14, v13, v12
	v_fma_f32 v15, -v11, v14, v13
	v_fmac_f32_e32 v14, v15, v12
	v_fma_f32 v11, -v11, v14, v13
	v_div_fmas_f32 v11, v11, v12, v14
	v_div_fixup_f32 v10, v11, v10, v113
	v_mul_f32_e32 v11, 0xbfb8aa3b, v117
	v_exp_f32_e32 v11, v11
	v_mul_f32_e32 v10, v97, v10
	v_add_f32_e32 v11, 1.0, v11
	v_div_scale_f32 v12, s[42:43], v11, v11, v117
	v_rcp_f32_e32 v13, v12
	s_nop 0
	v_fma_f32 v14, -v12, v13, 1.0
	v_fmac_f32_e32 v13, v14, v13
	v_div_scale_f32 v14, vcc, v117, v11, v117
	v_mul_f32_e32 v15, v14, v13
	v_fma_f32 v96, -v12, v15, v14
	v_fmac_f32_e32 v15, v96, v13
	v_fma_f32 v12, -v12, v15, v14
	v_div_fmas_f32 v12, v12, v13, v15
	v_div_fixup_f32 v11, v12, v11, v117
	v_mul_f32_e32 v12, 0xbfb8aa3b, v121
	v_exp_f32_e32 v12, v12
	v_mul_f32_e32 v11, v101, v11
	v_add_f32_e32 v12, 1.0, v12
	v_div_scale_f32 v13, s[42:43], v12, v12, v121
	v_rcp_f32_e32 v14, v13
	s_nop 0
	v_fma_f32 v15, -v13, v14, 1.0
	v_fmac_f32_e32 v14, v15, v14
	v_div_scale_f32 v15, vcc, v121, v12, v121
	v_mul_f32_e32 v96, v15, v14
	v_fma_f32 v97, -v13, v96, v15
	v_fmac_f32_e32 v96, v97, v14
	v_fma_f32 v13, -v13, v96, v15
	v_div_fmas_f32 v13, v13, v14, v96
	v_div_fixup_f32 v12, v13, v12, v121
	v_mul_f32_e32 v13, 0xbfb8aa3b, v125
	v_exp_f32_e32 v13, v13
	v_mul_f32_e32 v12, v105, v12
	v_add_f32_e32 v13, 1.0, v13
	v_div_scale_f32 v14, s[42:43], v13, v13, v125
	v_rcp_f32_e32 v15, v14
	s_nop 0
	v_fma_f32 v96, -v14, v15, 1.0
	v_fmac_f32_e32 v15, v96, v15
	v_div_scale_f32 v96, vcc, v125, v13, v125
	v_mul_f32_e32 v97, v96, v15
	v_fma_f32 v100, -v14, v97, v96
	v_fmac_f32_e32 v97, v100, v15
	v_fma_f32 v14, -v14, v97, v96
	v_div_fmas_f32 v14, v14, v15, v97
	v_div_fixup_f32 v13, v14, v13, v125
	v_mul_f32_e32 v14, 0xbfb8aa3b, v114
	v_exp_f32_e32 v14, v14
	v_mul_f32_e32 v13, v109, v13
	v_add_f32_e32 v14, 1.0, v14
	v_div_scale_f32 v15, s[42:43], v14, v14, v114
	v_rcp_f32_e32 v96, v15
	s_nop 0
	v_fma_f32 v97, -v15, v96, 1.0
	v_fmac_f32_e32 v96, v97, v96
	v_div_scale_f32 v97, vcc, v114, v14, v114
	v_mul_f32_e32 v100, v97, v96
	v_fma_f32 v101, -v15, v100, v97
	v_fmac_f32_e32 v100, v101, v96
	v_fma_f32 v15, -v15, v100, v97
	v_div_fmas_f32 v15, v15, v96, v100
	v_div_fixup_f32 v14, v15, v14, v114
	v_mul_f32_e32 v15, 0xbfb8aa3b, v118
	v_exp_f32_e32 v15, v15
	v_mul_f32_e32 v14, v98, v14
	v_add_f32_e32 v15, 1.0, v15
	v_div_scale_f32 v96, s[42:43], v15, v15, v118
	v_rcp_f32_e32 v97, v96
	s_nop 0
	v_fma_f32 v98, -v96, v97, 1.0
	v_fmac_f32_e32 v97, v98, v97
	v_div_scale_f32 v98, vcc, v118, v15, v118
	v_mul_f32_e32 v100, v98, v97
	v_fma_f32 v101, -v96, v100, v98
	v_fmac_f32_e32 v100, v101, v97
	v_fma_f32 v96, -v96, v100, v98
	v_div_fmas_f32 v96, v96, v97, v100
	v_div_fixup_f32 v15, v96, v15, v118
	v_mul_f32_e32 v96, 0xbfb8aa3b, v122
	v_exp_f32_e32 v96, v96
	v_mul_f32_e32 v15, v102, v15
	v_add_f32_e32 v96, 1.0, v96
	v_div_scale_f32 v97, s[42:43], v96, v96, v122
	v_rcp_f32_e32 v98, v97
	s_nop 0
	v_fma_f32 v100, -v97, v98, 1.0
	v_fmac_f32_e32 v98, v100, v98
	v_div_scale_f32 v100, vcc, v122, v96, v122
	v_mul_f32_e32 v101, v100, v98
	v_fma_f32 v102, -v97, v101, v100
	v_fmac_f32_e32 v101, v102, v98
	v_fma_f32 v97, -v97, v101, v100
	v_div_fmas_f32 v97, v97, v98, v101
	v_div_fixup_f32 v96, v97, v96, v122
	v_mul_f32_e32 v100, v106, v96
	v_mul_f32_e32 v96, 0xbfb8aa3b, v126
	v_exp_f32_e32 v96, v96
	s_nop 0
	v_add_f32_e32 v96, 1.0, v96
	v_div_scale_f32 v97, s[42:43], v96, v96, v126
	v_rcp_f32_e32 v98, v97
	s_nop 0
	v_fma_f32 v101, -v97, v98, 1.0
	v_fmac_f32_e32 v98, v101, v98
	v_div_scale_f32 v101, vcc, v126, v96, v126
	v_mul_f32_e32 v102, v101, v98
	v_fma_f32 v104, -v97, v102, v101
	v_fmac_f32_e32 v102, v104, v98
	v_fma_f32 v97, -v97, v102, v101
	v_div_fmas_f32 v97, v97, v98, v102
	v_div_fixup_f32 v96, v97, v96, v126
	v_mul_f32_e32 v101, v110, v96
	v_mul_f32_e32 v96, 0xbfb8aa3b, v115
	v_exp_f32_e32 v96, v96
	s_nop 0
	v_add_f32_e32 v96, 1.0, v96
	v_div_scale_f32 v97, s[42:43], v96, v96, v115
	v_rcp_f32_e32 v98, v97
	s_nop 0
	v_fma_f32 v102, -v97, v98, 1.0
	v_fmac_f32_e32 v98, v102, v98
	v_div_scale_f32 v102, vcc, v115, v96, v115
	v_mul_f32_e32 v104, v102, v98
	v_fma_f32 v105, -v97, v104, v102
	v_fmac_f32_e32 v104, v105, v98
	v_fma_f32 v97, -v97, v104, v102
	v_div_fmas_f32 v97, v97, v98, v104
	v_div_fixup_f32 v96, v97, v96, v115
	v_mul_f32_e32 v102, v99, v96
	v_mul_f32_e32 v96, 0xbfb8aa3b, v119
	v_exp_f32_e32 v96, v96
	s_nop 0
	v_add_f32_e32 v96, 1.0, v96
	v_div_scale_f32 v97, s[42:43], v96, v96, v119
	v_rcp_f32_e32 v98, v97
	s_nop 0
	v_fma_f32 v99, -v97, v98, 1.0
	v_fmac_f32_e32 v98, v99, v98
	v_div_scale_f32 v99, vcc, v119, v96, v119
	v_mul_f32_e32 v104, v99, v98
	v_fma_f32 v105, -v97, v104, v99
	v_fmac_f32_e32 v104, v105, v98
	v_fma_f32 v97, -v97, v104, v99
	v_div_fmas_f32 v97, v97, v98, v104
	v_div_fixup_f32 v96, v97, v96, v119
	v_mul_f32_e32 v103, v103, v96
	v_mul_f32_e32 v96, 0xbfb8aa3b, v123
	v_exp_f32_e32 v96, v96
	s_nop 0
	v_add_f32_e32 v96, 1.0, v96
	v_div_scale_f32 v97, s[42:43], v96, v96, v123
	v_rcp_f32_e32 v98, v97
	s_nop 0
	v_fma_f32 v99, -v97, v98, 1.0
	v_fmac_f32_e32 v98, v99, v98
	v_div_scale_f32 v99, vcc, v123, v96, v123
	v_mul_f32_e32 v104, v99, v98
	v_fma_f32 v105, -v97, v104, v99
	v_fmac_f32_e32 v104, v105, v98
	v_fma_f32 v97, -v97, v104, v99
	v_div_fmas_f32 v97, v97, v98, v104
	v_div_fixup_f32 v96, v97, v96, v123
	v_mul_f32_e32 v104, v107, v96
	v_mul_f32_e32 v96, 0xbfb8aa3b, v127
	v_exp_f32_e32 v96, v96
	s_nop 0
	v_add_f32_e32 v96, 1.0, v96
	v_div_scale_f32 v97, s[42:43], v96, v96, v127
	v_rcp_f32_e32 v98, v97
	s_nop 0
	v_fma_f32 v99, -v97, v98, 1.0
	v_fmac_f32_e32 v98, v99, v98
	v_div_scale_f32 v99, vcc, v127, v96, v127
	v_mul_f32_e32 v105, v99, v98
	v_fma_f32 v106, -v97, v105, v99
	v_fmac_f32_e32 v105, v106, v98
	v_fma_f32 v97, -v97, v105, v99
	v_div_fmas_f32 v97, v97, v98, v105
	v_div_fixup_f32 v96, v97, v96, v127
	v_mul_f32_e32 v105, v111, v96
	v_mov_b32_e32 v96, v1
	v_mov_b32_e32 v97, v1
	v_mov_b32_e32 v98, v1
	v_mov_b32_e32 v99, v1
	v_cvt_pk_fp8_f32 v96, v0, v7
	v_cvt_pk_fp8_f32 v97, v10, v11
	v_cvt_pk_fp8_f32 v98, v14, v15
	v_cvt_pk_fp8_f32 v99, v102, v103
	v_cvt_pk_fp8_f32 v96, v8, v9 op_sel:[0,0,1]
	v_cvt_pk_fp8_f32 v97, v12, v13 op_sel:[0,0,1]
	v_cvt_pk_fp8_f32 v98, v100, v101 op_sel:[0,0,1]
	v_cvt_pk_fp8_f32 v99, v104, v105 op_sel:[0,0,1]
	s_andn2_b64 vcc, exec, s[44:45]
	global_store_dwordx4 v[4:5], v[96:99], off offset:32
	s_cbranch_vccnz .LBB0_1314
	ds_read_b32 v0, v6 offset:55424
	s_waitcnt lgkmcnt(0)
	v_lshlrev_b64 v[4:5], 8, v[0:1]
	v_mul_f32_e32 v0, 0xbfb8aa3b, v80
	v_exp_f32_e32 v0, v0
	v_lshl_add_u64 v[2:3], v[2:3], 0, v[4:5]
	v_add_f32_e32 v0, 1.0, v0
	v_div_scale_f32 v4, s[42:43], v0, v0, v80
	v_rcp_f32_e32 v5, v4
	s_nop 0
	v_fma_f32 v6, -v4, v5, 1.0
	v_fmac_f32_e32 v5, v6, v5
	v_div_scale_f32 v6, vcc, v80, v0, v80
	v_mul_f32_e32 v7, v6, v5
	v_fma_f32 v8, -v4, v7, v6
	v_fmac_f32_e32 v7, v8, v5
	v_fma_f32 v4, -v4, v7, v6
	v_div_fmas_f32 v4, v4, v5, v7
	v_div_fixup_f32 v0, v4, v0, v80
	v_mul_f32_e32 v4, 0xbfb8aa3b, v84
	v_exp_f32_e32 v4, v4
	v_mul_f32_e32 v0, v64, v0
	v_add_f32_e32 v4, 1.0, v4
	v_div_scale_f32 v5, s[42:43], v4, v4, v84
	v_rcp_f32_e32 v6, v5
	s_nop 0
	v_fma_f32 v7, -v5, v6, 1.0
	v_fmac_f32_e32 v6, v7, v6
	v_div_scale_f32 v7, vcc, v84, v4, v84
	v_mul_f32_e32 v8, v7, v6
	v_fma_f32 v9, -v5, v8, v7
	v_fmac_f32_e32 v8, v9, v6
	v_fma_f32 v5, -v5, v8, v7
	v_div_fmas_f32 v5, v5, v6, v8
	v_div_fixup_f32 v4, v5, v4, v84
	v_mul_f32_e32 v5, 0xbfb8aa3b, v88
	v_exp_f32_e32 v5, v5
	v_mul_f32_e32 v4, v68, v4
	v_add_f32_e32 v5, 1.0, v5
	v_div_scale_f32 v6, s[42:43], v5, v5, v88
	v_rcp_f32_e32 v7, v6
	s_nop 0
	v_fma_f32 v8, -v6, v7, 1.0
	v_fmac_f32_e32 v7, v8, v7
	v_div_scale_f32 v8, vcc, v88, v5, v88
	v_mul_f32_e32 v9, v8, v7
	v_fma_f32 v10, -v6, v9, v8
	v_fmac_f32_e32 v9, v10, v7
	v_fma_f32 v6, -v6, v9, v8
	v_div_fmas_f32 v6, v6, v7, v9
	v_div_fixup_f32 v5, v6, v5, v88
	v_mul_f32_e32 v6, 0xbfb8aa3b, v92
	v_exp_f32_e32 v6, v6
	v_mul_f32_e32 v5, v72, v5
	v_add_f32_e32 v6, 1.0, v6
	v_div_scale_f32 v7, s[42:43], v6, v6, v92
	v_rcp_f32_e32 v8, v7
	s_nop 0
	v_fma_f32 v9, -v7, v8, 1.0
	v_fmac_f32_e32 v8, v9, v8
	v_div_scale_f32 v9, vcc, v92, v6, v92
	v_mul_f32_e32 v10, v9, v8
	v_fma_f32 v11, -v7, v10, v9
	v_fmac_f32_e32 v10, v11, v8
	v_fma_f32 v7, -v7, v10, v9
	v_div_fmas_f32 v7, v7, v8, v10
	v_div_fixup_f32 v6, v7, v6, v92
	v_mul_f32_e32 v7, 0xbfb8aa3b, v81
	v_exp_f32_e32 v7, v7
	v_mul_f32_e32 v6, v76, v6
	v_add_f32_e32 v7, 1.0, v7
	v_div_scale_f32 v8, s[42:43], v7, v7, v81
	v_rcp_f32_e32 v9, v8
	s_nop 0
	v_fma_f32 v10, -v8, v9, 1.0
	v_fmac_f32_e32 v9, v10, v9
	v_div_scale_f32 v10, vcc, v81, v7, v81
	v_mul_f32_e32 v11, v10, v9
	v_fma_f32 v12, -v8, v11, v10
	v_fmac_f32_e32 v11, v12, v9
	v_fma_f32 v8, -v8, v11, v10
	v_div_fmas_f32 v8, v8, v9, v11
	v_div_fixup_f32 v7, v8, v7, v81
	v_mul_f32_e32 v8, 0xbfb8aa3b, v85
	v_exp_f32_e32 v8, v8
	v_mul_f32_e32 v7, v65, v7
	v_add_f32_e32 v8, 1.0, v8
	v_div_scale_f32 v9, s[42:43], v8, v8, v85
	v_rcp_f32_e32 v10, v9
	s_nop 0
	v_fma_f32 v11, -v9, v10, 1.0
	v_fmac_f32_e32 v10, v11, v10
	v_div_scale_f32 v11, vcc, v85, v8, v85
	v_mul_f32_e32 v12, v11, v10
	v_fma_f32 v13, -v9, v12, v11
	v_fmac_f32_e32 v12, v13, v10
	v_fma_f32 v9, -v9, v12, v11
	v_div_fmas_f32 v9, v9, v10, v12
	v_div_fixup_f32 v8, v9, v8, v85
	v_mul_f32_e32 v9, 0xbfb8aa3b, v89
	v_exp_f32_e32 v9, v9
	v_mul_f32_e32 v8, v69, v8
	v_add_f32_e32 v9, 1.0, v9
	v_div_scale_f32 v10, s[42:43], v9, v9, v89
	v_rcp_f32_e32 v11, v10
	s_nop 0
	v_fma_f32 v12, -v10, v11, 1.0
	v_fmac_f32_e32 v11, v12, v11
	v_div_scale_f32 v12, vcc, v89, v9, v89
	v_mul_f32_e32 v13, v12, v11
	v_fma_f32 v14, -v10, v13, v12
	v_fmac_f32_e32 v13, v14, v11
	v_fma_f32 v10, -v10, v13, v12
	v_div_fmas_f32 v10, v10, v11, v13
	v_div_fixup_f32 v9, v10, v9, v89
	v_mul_f32_e32 v10, 0xbfb8aa3b, v93
	v_exp_f32_e32 v10, v10
	v_mul_f32_e32 v9, v73, v9
	v_add_f32_e32 v10, 1.0, v10
	v_div_scale_f32 v11, s[42:43], v10, v10, v93
	v_rcp_f32_e32 v12, v11
	s_nop 0
	v_fma_f32 v13, -v11, v12, 1.0
	v_fmac_f32_e32 v12, v13, v12
	v_div_scale_f32 v13, vcc, v93, v10, v93
	v_mul_f32_e32 v14, v13, v12
	v_fma_f32 v15, -v11, v14, v13
	v_fmac_f32_e32 v14, v15, v12
	v_fma_f32 v11, -v11, v14, v13
	v_div_fmas_f32 v11, v11, v12, v14
	v_div_fixup_f32 v10, v11, v10, v93
	v_mul_f32_e32 v11, 0xbfb8aa3b, v82
	v_exp_f32_e32 v11, v11
	v_mul_f32_e32 v10, v77, v10
	v_add_f32_e32 v11, 1.0, v11
	v_div_scale_f32 v12, s[42:43], v11, v11, v82
	v_rcp_f32_e32 v13, v12
	s_nop 0
	v_fma_f32 v14, -v12, v13, 1.0
	v_fmac_f32_e32 v13, v14, v13
	v_div_scale_f32 v14, vcc, v82, v11, v82
	v_mul_f32_e32 v15, v14, v13
	v_fma_f32 v64, -v12, v15, v14
	v_fmac_f32_e32 v15, v64, v13
	v_fma_f32 v12, -v12, v15, v14
	v_div_fmas_f32 v12, v12, v13, v15
	v_div_fixup_f32 v11, v12, v11, v82
	v_mul_f32_e32 v12, 0xbfb8aa3b, v86
	v_exp_f32_e32 v12, v12
	v_mul_f32_e32 v11, v66, v11
	v_add_f32_e32 v12, 1.0, v12
	v_div_scale_f32 v13, s[42:43], v12, v12, v86
	v_rcp_f32_e32 v14, v13
	s_nop 0
	v_fma_f32 v15, -v13, v14, 1.0
	v_fmac_f32_e32 v14, v15, v14
	v_div_scale_f32 v15, vcc, v86, v12, v86
	v_mul_f32_e32 v64, v15, v14
	v_fma_f32 v65, -v13, v64, v15
	v_fmac_f32_e32 v64, v65, v14
	v_fma_f32 v13, -v13, v64, v15
	v_div_fmas_f32 v13, v13, v14, v64
	v_div_fixup_f32 v12, v13, v12, v86
	v_mul_f32_e32 v15, v70, v12
	v_mul_f32_e32 v12, 0xbfb8aa3b, v90
	v_exp_f32_e32 v12, v12
	s_nop 0
	v_add_f32_e32 v12, 1.0, v12
	v_div_scale_f32 v13, s[42:43], v12, v12, v90
	v_rcp_f32_e32 v14, v13
	s_nop 0
	v_fma_f32 v64, -v13, v14, 1.0
	v_fmac_f32_e32 v14, v64, v14
	v_div_scale_f32 v64, vcc, v90, v12, v90
	v_mul_f32_e32 v65, v64, v14
	v_fma_f32 v66, -v13, v65, v64
	v_fmac_f32_e32 v65, v66, v14
	v_fma_f32 v13, -v13, v65, v64
	v_div_fmas_f32 v13, v13, v14, v65
	v_div_fixup_f32 v12, v13, v12, v90
	v_mul_f32_e32 v64, v74, v12
	v_mul_f32_e32 v12, 0xbfb8aa3b, v94
	v_exp_f32_e32 v12, v12
	s_nop 0
	v_add_f32_e32 v12, 1.0, v12
	v_div_scale_f32 v13, s[42:43], v12, v12, v94
	v_rcp_f32_e32 v14, v13
	s_nop 0
	v_fma_f32 v65, -v13, v14, 1.0
	v_fmac_f32_e32 v14, v65, v14
	v_div_scale_f32 v65, vcc, v94, v12, v94
	v_mul_f32_e32 v66, v65, v14
	v_fma_f32 v68, -v13, v66, v65
	v_fmac_f32_e32 v66, v68, v14
	v_fma_f32 v13, -v13, v66, v65
	v_div_fmas_f32 v13, v13, v14, v66
	v_div_fixup_f32 v12, v13, v12, v94
	v_mul_f32_e32 v65, v78, v12
	v_mul_f32_e32 v12, 0xbfb8aa3b, v83
	v_exp_f32_e32 v12, v12
	s_nop 0
	v_add_f32_e32 v12, 1.0, v12
	v_div_scale_f32 v13, s[42:43], v12, v12, v83
	v_rcp_f32_e32 v14, v13
	s_nop 0
	v_fma_f32 v66, -v13, v14, 1.0
	v_fmac_f32_e32 v14, v66, v14
	v_div_scale_f32 v66, vcc, v83, v12, v83
	v_mul_f32_e32 v68, v66, v14
	v_fma_f32 v69, -v13, v68, v66
	v_fmac_f32_e32 v68, v69, v14
	v_fma_f32 v13, -v13, v68, v66
	v_div_fmas_f32 v13, v13, v14, v68
	v_div_fixup_f32 v12, v13, v12, v83
	v_mul_f32_e32 v66, v67, v12
	v_mul_f32_e32 v12, 0xbfb8aa3b, v87
	v_exp_f32_e32 v12, v12
	s_nop 0
	v_add_f32_e32 v12, 1.0, v12
	v_div_scale_f32 v13, s[42:43], v12, v12, v87
	v_rcp_f32_e32 v14, v13
	s_nop 0
	v_fma_f32 v67, -v13, v14, 1.0
	v_fmac_f32_e32 v14, v67, v14
	v_div_scale_f32 v67, vcc, v87, v12, v87
	v_mul_f32_e32 v68, v67, v14
	v_fma_f32 v69, -v13, v68, v67
	v_fmac_f32_e32 v68, v69, v14
	v_fma_f32 v13, -v13, v68, v67
	v_div_fmas_f32 v13, v13, v14, v68
	v_div_fixup_f32 v12, v13, v12, v87
	v_mul_f32_e32 v67, v71, v12
	v_mul_f32_e32 v12, 0xbfb8aa3b, v91
	v_exp_f32_e32 v12, v12
	s_nop 0
	v_add_f32_e32 v12, 1.0, v12
	v_div_scale_f32 v13, s[42:43], v12, v12, v91
	v_rcp_f32_e32 v14, v13
	s_nop 0
	v_fma_f32 v68, -v13, v14, 1.0
	v_fmac_f32_e32 v14, v68, v14
	v_div_scale_f32 v68, vcc, v91, v12, v91
	v_mul_f32_e32 v69, v68, v14
	v_fma_f32 v70, -v13, v69, v68
	v_fmac_f32_e32 v69, v70, v14
	v_fma_f32 v13, -v13, v69, v68
	v_div_fmas_f32 v13, v13, v14, v69
	v_div_fixup_f32 v12, v13, v12, v91
	v_mul_f32_e32 v68, v75, v12
	v_mul_f32_e32 v12, 0xbfb8aa3b, v95
	v_exp_f32_e32 v12, v12
	s_nop 0
	v_add_f32_e32 v12, 1.0, v12
	v_div_scale_f32 v13, s[42:43], v12, v12, v95
	v_rcp_f32_e32 v14, v13
	s_nop 0
	v_fma_f32 v69, -v13, v14, 1.0
	v_fmac_f32_e32 v14, v69, v14
	v_div_scale_f32 v69, vcc, v95, v12, v95
	v_mul_f32_e32 v70, v69, v14
	v_fma_f32 v71, -v13, v70, v69
	v_fmac_f32_e32 v70, v71, v14
	v_fma_f32 v13, -v13, v70, v69
	v_div_fmas_f32 v13, v13, v14, v70
	v_div_fixup_f32 v12, v13, v12, v95
	v_mul_f32_e32 v69, v79, v12
	v_mov_b32_e32 v12, v1
	v_cvt_pk_fp8_f32 v12, v0, v4
	v_mul_f32_e32 v0, 0xbfb8aa3b, v48
	v_exp_f32_e32 v0, v0
	v_mov_b32_e32 v13, v1
	v_cvt_pk_fp8_f32 v12, v5, v6 op_sel:[0,0,1]
	v_cvt_pk_fp8_f32 v13, v7, v8
	v_add_f32_e32 v0, 1.0, v0
	v_div_scale_f32 v4, s[42:43], v0, v0, v48
	v_rcp_f32_e32 v5, v4
	v_cvt_pk_fp8_f32 v13, v9, v10 op_sel:[0,0,1]
	v_mov_b32_e32 v14, v1
	v_cvt_pk_fp8_f32 v14, v11, v15
	v_fma_f32 v6, -v4, v5, 1.0
	v_fmac_f32_e32 v5, v6, v5
	v_div_scale_f32 v6, vcc, v48, v0, v48
	v_mul_f32_e32 v7, v6, v5
	v_fma_f32 v8, -v4, v7, v6
	v_fmac_f32_e32 v7, v8, v5
	v_fma_f32 v4, -v4, v7, v6
	v_div_fmas_f32 v4, v4, v5, v7
	v_div_fixup_f32 v0, v4, v0, v48
	v_mul_f32_e32 v4, 0xbfb8aa3b, v52
	v_exp_f32_e32 v4, v4
	v_mov_b32_e32 v15, v1
	v_cvt_pk_fp8_f32 v15, v66, v67
	v_cvt_pk_fp8_f32 v14, v64, v65 op_sel:[0,0,1]
	v_add_f32_e32 v4, 1.0, v4
	v_div_scale_f32 v5, s[42:43], v4, v4, v52
	v_rcp_f32_e32 v6, v5
	v_cvt_pk_fp8_f32 v15, v68, v69 op_sel:[0,0,1]
	v_mul_f32_e32 v0, v32, v0
	v_fma_f32 v7, -v5, v6, 1.0
	v_fmac_f32_e32 v6, v7, v6
	v_div_scale_f32 v7, vcc, v52, v4, v52
	v_mul_f32_e32 v8, v7, v6
	v_fma_f32 v9, -v5, v8, v7
	v_fmac_f32_e32 v8, v9, v6
	v_fma_f32 v5, -v5, v8, v7
	v_div_fmas_f32 v5, v5, v6, v8
	v_div_fixup_f32 v4, v5, v4, v52
	v_mul_f32_e32 v5, 0xbfb8aa3b, v56
	v_exp_f32_e32 v5, v5
	global_store_dwordx4 v[2:3], v[12:15], off
	v_mul_f32_e32 v4, v36, v4
	v_add_f32_e32 v5, 1.0, v5
	v_div_scale_f32 v6, s[42:43], v5, v5, v56
	v_rcp_f32_e32 v7, v6
	s_nop 0
	v_fma_f32 v8, -v6, v7, 1.0
	v_fmac_f32_e32 v7, v8, v7
	v_div_scale_f32 v8, vcc, v56, v5, v56
	v_mul_f32_e32 v9, v8, v7
	v_fma_f32 v10, -v6, v9, v8
	v_fmac_f32_e32 v9, v10, v7
	v_fma_f32 v6, -v6, v9, v8
	v_div_fmas_f32 v6, v6, v7, v9
	v_div_fixup_f32 v5, v6, v5, v56
	v_mul_f32_e32 v6, 0xbfb8aa3b, v60
	v_exp_f32_e32 v6, v6
	v_mul_f32_e32 v5, v40, v5
	v_add_f32_e32 v6, 1.0, v6
	v_div_scale_f32 v7, s[42:43], v6, v6, v60
	v_rcp_f32_e32 v8, v7
	s_nop 0
	v_fma_f32 v9, -v7, v8, 1.0
	v_fmac_f32_e32 v8, v9, v8
	v_div_scale_f32 v9, vcc, v60, v6, v60
	v_mul_f32_e32 v10, v9, v8
	v_fma_f32 v11, -v7, v10, v9
	v_fmac_f32_e32 v10, v11, v8
	v_fma_f32 v7, -v7, v10, v9
	v_div_fmas_f32 v7, v7, v8, v10
	v_div_fixup_f32 v6, v7, v6, v60
	v_mul_f32_e32 v7, 0xbfb8aa3b, v49
	v_exp_f32_e32 v7, v7
	v_mul_f32_e32 v6, v44, v6
	v_add_f32_e32 v7, 1.0, v7
	v_div_scale_f32 v8, s[42:43], v7, v7, v49
	v_rcp_f32_e32 v9, v8
	s_nop 0
	v_fma_f32 v10, -v8, v9, 1.0
	v_fmac_f32_e32 v9, v10, v9
	v_div_scale_f32 v10, vcc, v49, v7, v49
	v_mul_f32_e32 v11, v10, v9
	v_fma_f32 v12, -v8, v11, v10
	v_fmac_f32_e32 v11, v12, v9
	v_fma_f32 v8, -v8, v11, v10
	v_div_fmas_f32 v8, v8, v9, v11
	v_div_fixup_f32 v7, v8, v7, v49
	v_mul_f32_e32 v8, 0xbfb8aa3b, v53
	v_exp_f32_e32 v8, v8
	v_mul_f32_e32 v7, v33, v7
	v_add_f32_e32 v8, 1.0, v8
	v_div_scale_f32 v9, s[42:43], v8, v8, v53
	v_rcp_f32_e32 v10, v9
	s_nop 0
	v_fma_f32 v11, -v9, v10, 1.0
	v_fmac_f32_e32 v10, v11, v10
	v_div_scale_f32 v11, vcc, v53, v8, v53
	v_mul_f32_e32 v12, v11, v10
	v_fma_f32 v13, -v9, v12, v11
	v_fmac_f32_e32 v12, v13, v10
	v_fma_f32 v9, -v9, v12, v11
	v_div_fmas_f32 v9, v9, v10, v12
	v_div_fixup_f32 v8, v9, v8, v53
	v_mul_f32_e32 v9, 0xbfb8aa3b, v57
	v_exp_f32_e32 v9, v9
	v_mul_f32_e32 v8, v37, v8
	v_add_f32_e32 v9, 1.0, v9
	v_div_scale_f32 v10, s[42:43], v9, v9, v57
	v_rcp_f32_e32 v11, v10
	s_nop 0
	v_fma_f32 v12, -v10, v11, 1.0
	v_fmac_f32_e32 v11, v12, v11
	v_div_scale_f32 v12, vcc, v57, v9, v57
	v_mul_f32_e32 v13, v12, v11
	v_fma_f32 v14, -v10, v13, v12
	v_fmac_f32_e32 v13, v14, v11
	v_fma_f32 v10, -v10, v13, v12
	v_div_fmas_f32 v10, v10, v11, v13
	v_div_fixup_f32 v9, v10, v9, v57
	v_mul_f32_e32 v10, 0xbfb8aa3b, v61
	v_exp_f32_e32 v10, v10
	v_mul_f32_e32 v9, v41, v9
	v_add_f32_e32 v10, 1.0, v10
	v_div_scale_f32 v11, s[42:43], v10, v10, v61
	v_rcp_f32_e32 v12, v11
	s_nop 0
	v_fma_f32 v13, -v11, v12, 1.0
	v_fmac_f32_e32 v12, v13, v12
	v_div_scale_f32 v13, vcc, v61, v10, v61
	v_mul_f32_e32 v14, v13, v12
	v_fma_f32 v15, -v11, v14, v13
	v_fmac_f32_e32 v14, v15, v12
	v_fma_f32 v11, -v11, v14, v13
	v_div_fmas_f32 v11, v11, v12, v14
	v_div_fixup_f32 v10, v11, v10, v61
	v_mul_f32_e32 v11, 0xbfb8aa3b, v50
	v_exp_f32_e32 v11, v11
	v_mul_f32_e32 v10, v45, v10
	v_add_f32_e32 v11, 1.0, v11
	v_div_scale_f32 v12, s[42:43], v11, v11, v50
	v_rcp_f32_e32 v13, v12
	s_nop 0
	v_fma_f32 v14, -v12, v13, 1.0
	v_fmac_f32_e32 v13, v14, v13
	v_div_scale_f32 v14, vcc, v50, v11, v50
	v_mul_f32_e32 v15, v14, v13
	v_fma_f32 v32, -v12, v15, v14
	v_fmac_f32_e32 v15, v32, v13
	v_fma_f32 v12, -v12, v15, v14
	v_div_fmas_f32 v12, v12, v13, v15
	v_div_fixup_f32 v11, v12, v11, v50
	v_mul_f32_e32 v12, 0xbfb8aa3b, v54
	v_exp_f32_e32 v12, v12
	v_mul_f32_e32 v11, v34, v11
	v_add_f32_e32 v12, 1.0, v12
	v_div_scale_f32 v13, s[42:43], v12, v12, v54
	v_rcp_f32_e32 v14, v13
	s_nop 0
	v_fma_f32 v15, -v13, v14, 1.0
	v_fmac_f32_e32 v14, v15, v14
	v_div_scale_f32 v15, vcc, v54, v12, v54
	v_mul_f32_e32 v32, v15, v14
	v_fma_f32 v33, -v13, v32, v15
	v_fmac_f32_e32 v32, v33, v14
	v_fma_f32 v13, -v13, v32, v15
	v_div_fmas_f32 v13, v13, v14, v32
	v_div_fixup_f32 v12, v13, v12, v54
	v_mul_f32_e32 v15, v38, v12
	v_mul_f32_e32 v12, 0xbfb8aa3b, v58
	v_exp_f32_e32 v12, v12
	s_nop 0
	v_add_f32_e32 v12, 1.0, v12
	v_div_scale_f32 v13, s[42:43], v12, v12, v58
	v_rcp_f32_e32 v14, v13
	s_nop 0
	v_fma_f32 v32, -v13, v14, 1.0
	v_fmac_f32_e32 v14, v32, v14
	v_div_scale_f32 v32, vcc, v58, v12, v58
	v_mul_f32_e32 v33, v32, v14
	v_fma_f32 v34, -v13, v33, v32
	v_fmac_f32_e32 v33, v34, v14
	v_fma_f32 v13, -v13, v33, v32
	v_div_fmas_f32 v13, v13, v14, v33
	v_div_fixup_f32 v12, v13, v12, v58
	v_mul_f32_e32 v32, v42, v12
	v_mul_f32_e32 v12, 0xbfb8aa3b, v62
	v_exp_f32_e32 v12, v12
	s_nop 0
	v_add_f32_e32 v12, 1.0, v12
	v_div_scale_f32 v13, s[42:43], v12, v12, v62
	v_rcp_f32_e32 v14, v13
	s_nop 0
	v_fma_f32 v33, -v13, v14, 1.0
	v_fmac_f32_e32 v14, v33, v14
	v_div_scale_f32 v33, vcc, v62, v12, v62
	v_mul_f32_e32 v34, v33, v14
	v_fma_f32 v36, -v13, v34, v33
	v_fmac_f32_e32 v34, v36, v14
	v_fma_f32 v13, -v13, v34, v33
	v_div_fmas_f32 v13, v13, v14, v34
	v_div_fixup_f32 v12, v13, v12, v62
	v_mul_f32_e32 v33, v46, v12
	v_mul_f32_e32 v12, 0xbfb8aa3b, v51
	v_exp_f32_e32 v12, v12
	s_nop 0
	v_add_f32_e32 v12, 1.0, v12
	v_div_scale_f32 v13, s[42:43], v12, v12, v51
	v_rcp_f32_e32 v14, v13
	s_nop 0
	v_fma_f32 v34, -v13, v14, 1.0
	v_fmac_f32_e32 v14, v34, v14
	v_div_scale_f32 v34, vcc, v51, v12, v51
	v_mul_f32_e32 v36, v34, v14
	v_fma_f32 v37, -v13, v36, v34
	v_fmac_f32_e32 v36, v37, v14
	v_fma_f32 v13, -v13, v36, v34
	v_div_fmas_f32 v13, v13, v14, v36
	v_div_fixup_f32 v12, v13, v12, v51
	v_mul_f32_e32 v34, v35, v12
	v_mul_f32_e32 v12, 0xbfb8aa3b, v55
	v_exp_f32_e32 v12, v12
	s_nop 0
	v_add_f32_e32 v12, 1.0, v12
	v_div_scale_f32 v13, s[42:43], v12, v12, v55
	v_rcp_f32_e32 v14, v13
	s_nop 0
	v_fma_f32 v35, -v13, v14, 1.0
	v_fmac_f32_e32 v14, v35, v14
	v_div_scale_f32 v35, vcc, v55, v12, v55
	v_mul_f32_e32 v36, v35, v14
	v_fma_f32 v37, -v13, v36, v35
	v_fmac_f32_e32 v36, v37, v14
	v_fma_f32 v13, -v13, v36, v35
	v_div_fmas_f32 v13, v13, v14, v36
	v_div_fixup_f32 v12, v13, v12, v55
	v_mul_f32_e32 v35, v39, v12
	v_mul_f32_e32 v12, 0xbfb8aa3b, v59
	v_exp_f32_e32 v12, v12
	s_nop 0
	v_add_f32_e32 v12, 1.0, v12
	v_div_scale_f32 v13, s[42:43], v12, v12, v59
	v_rcp_f32_e32 v14, v13
	s_nop 0
	v_fma_f32 v36, -v13, v14, 1.0
	v_fmac_f32_e32 v14, v36, v14
	v_div_scale_f32 v36, vcc, v59, v12, v59
	v_mul_f32_e32 v37, v36, v14
	v_fma_f32 v38, -v13, v37, v36
	v_fmac_f32_e32 v37, v38, v14
	v_fma_f32 v13, -v13, v37, v36
	v_div_fmas_f32 v13, v13, v14, v37
	v_div_fixup_f32 v12, v13, v12, v59
	v_mul_f32_e32 v36, v43, v12
	v_mul_f32_e32 v12, 0xbfb8aa3b, v63
	v_exp_f32_e32 v12, v12
	s_nop 0
	v_add_f32_e32 v12, 1.0, v12
	v_div_scale_f32 v13, s[42:43], v12, v12, v63
	v_rcp_f32_e32 v14, v13
	s_nop 0
	v_fma_f32 v37, -v13, v14, 1.0
	v_fmac_f32_e32 v14, v37, v14
	v_div_scale_f32 v37, vcc, v63, v12, v63
	v_mul_f32_e32 v38, v37, v14
	v_fma_f32 v39, -v13, v38, v37
	v_fmac_f32_e32 v38, v39, v14
	v_fma_f32 v13, -v13, v38, v37
	v_div_fmas_f32 v13, v13, v14, v38
	v_div_fixup_f32 v12, v13, v12, v63
	v_mov_b32_e32 v14, v1
	v_mul_f32_e32 v37, v47, v12
	v_mov_b32_e32 v12, v1
	v_mov_b32_e32 v13, v1
	v_cvt_pk_fp8_f32 v14, v11, v15
	v_mov_b32_e32 v15, v1
	v_cvt_pk_fp8_f32 v12, v0, v4
	v_cvt_pk_fp8_f32 v13, v7, v8
	v_cvt_pk_fp8_f32 v15, v34, v35
	v_cvt_pk_fp8_f32 v14, v32, v33 op_sel:[0,0,1]
	v_cvt_pk_fp8_f32 v12, v5, v6 op_sel:[0,0,1]
	v_cvt_pk_fp8_f32 v13, v9, v10 op_sel:[0,0,1]
	v_cvt_pk_fp8_f32 v15, v36, v37 op_sel:[0,0,1]
	global_store_dwordx4 v[2:3], v[12:15], off offset:32

.Lgu_es:
	s_waitcnt vmcnt(12)
	v_cvt_pk_bf16_f32 v2, v144, v148
	v_cvt_pk_bf16_f32 v3, v152, v156
	s_lshl_b64 s[0:1], s[56:57], 2
	s_waitcnt lgkmcnt(0)
	s_barrier
	ds_write2_b32 v0, v2, v3 offset1:8
	v_cvt_pk_bf16_f32 v2, v145, v149
	v_cvt_pk_bf16_f32 v3, v153, v157
	v_add_u32_e32 v4, 0x400, v0
	s_add_u32 s0, s11, s0
	ds_write2_b32 v4, v2, v3 offset0:32 offset1:40
	v_cvt_pk_bf16_f32 v2, v146, v150
	v_cvt_pk_bf16_f32 v3, v154, v158
	v_add_u32_e32 v4, 0x800, v0
	s_addc_u32 s1, s79, s1
	ds_write2_b32 v4, v2, v3 offset0:64 offset1:72
	v_cvt_pk_bf16_f32 v2, v147, v151
	v_cvt_pk_bf16_f32 v3, v155, v159
	v_add_u32_e32 v0, 0xc00, v0
	s_add_u32 s46, s0, 0x4000
	ds_write2_b32 v0, v2, v3 offset0:96 offset1:104
	s_addc_u32 s47, s1, 0
	v_mov_b32_e32 v0, v192
	global_load_dwordx4 v[144:147], v0, s[0:1] nt
	global_load_dwordx4 v[148:151], v0, s[0:1] offset:1024 nt
	global_load_dwordx4 v[152:155], v0, s[46:47] nt
	global_load_dwordx4 v[156:159], v0, s[46:47] offset:1024 nt
	s_sub_i32 s1, s2, 64
	s_add_i32 s0, s49, -1
	s_and_b32 s1, s1, 0x3c0
	s_cmp_lt_u32 s0, s40
	s_cselect_b32 s0, s1, 0
	s_add_u32 s46, s0, s54
	v_cndmask_b32_e64 v0, 0, 1, s[42:43]
	s_addc_u32 s47, 0, s55
	v_cmp_ne_u32_e64 s[0:1], 1, v0
	s_andn2_b64 vcc, exec, s[42:43]
	s_cbranch_vccnz .LBB0_1326
	s_waitcnt vmcnt(14)
	s_mul_i32 s25, s29, 0x4800
	v_add_u32_e32 v0, s25, v197
	ds_read_b128 v[2:5], v0
	v_cvt_scalef32_pk_bf16_fp8 v6, v188, 1.0
	v_cvt_scalef32_pk_bf16_fp8 v7, v188, 1.0 op_sel:[1,0,0]
	v_cvt_scalef32_pk_bf16_fp8 v8, v189, 1.0
	v_cvt_scalef32_pk_bf16_fp8 v9, v189, 1.0 op_sel:[1,0,0]
	ds_read_b128 v[10:13], v0 offset:4608
	ds_read_b128 v[198:201], v0 offset:9216
	ds_read_b128 v[202:205], v0 offset:13824
	s_waitcnt lgkmcnt(3)
	v_mfma_f32_32x32x16_bf16 v[128:143], v[2:5], v[6:9], v[128:143]
	s_waitcnt vmcnt(12)
	v_cvt_pk_f32_fp8_e32 v[14:15], v185
	s_waitcnt lgkmcnt(2)
	v_mfma_f32_32x32x16_bf16 v[96:111], v[10:13], v[6:9], v[96:111]
	s_waitcnt lgkmcnt(1)
	v_mfma_f32_32x32x16_bf16 v[112:127], v[198:201], v[6:9], v[112:127]
	s_waitcnt lgkmcnt(0)
	v_mfma_f32_32x32x16_bf16 v[80:95], v[202:205], v[6:9], v[80:95]
	v_cvt_pk_f32_fp8_e32 v[6:7], v184
	v_cvt_pk_f32_fp8_sdwa v[8:9], v184 src0_sel:WORD_1
	v_cvt_pk_f32_fp8_sdwa v[184:185], v185 src0_sel:WORD_1
	v_cvt_pk_bf16_f32 v6, v6, v7
	v_cvt_pk_bf16_f32 v7, v8, v9
	v_cvt_pk_bf16_f32 v8, v14, v15
	v_cvt_pk_bf16_f32 v9, v184, v185
	s_nop 1
	v_mfma_f32_32x32x16_bf16 v[64:79], v[2:5], v[6:9], v[64:79]
	ds_read_b128 v[2:5], v0 offset:16
	v_mfma_f32_32x32x16_bf16 v[32:47], v[10:13], v[6:9], v[32:47]
	v_cvt_pk_f32_fp8_e32 v[10:11], v191
	v_cvt_pk_f32_fp8_sdwa v[12:13], v191 src0_sel:WORD_1
	v_mfma_f32_32x32x16_bf16 v[48:63], v[198:201], v[6:9], v[48:63]
	ds_read_b128 v[198:201], v0 offset:13840
	v_mfma_f32_32x32x16_bf16 v[16:31], v[202:205], v[6:9], v[16:31]
	v_cvt_pk_f32_fp8_e32 v[6:7], v190
	v_cvt_pk_f32_fp8_sdwa v[8:9], v190 src0_sel:WORD_1
	ds_read_b128 v[188:191], v0 offset:9232
	v_cvt_pk_bf16_f32 v6, v6, v7
	v_cvt_pk_bf16_f32 v7, v8, v9
	v_cvt_pk_bf16_f32 v8, v10, v11
	v_cvt_pk_bf16_f32 v9, v12, v13
	ds_read_b128 v[10:13], v0 offset:4624
	s_waitcnt lgkmcnt(3)
	v_mfma_f32_32x32x16_bf16 v[128:143], v[2:5], v[6:9], v[128:143]
	s_waitcnt lgkmcnt(0)
	v_mfma_f32_32x32x16_bf16 v[96:111], v[10:13], v[6:9], v[96:111]
	v_mfma_f32_32x32x16_bf16 v[112:127], v[188:191], v[6:9], v[112:127]
	v_mfma_f32_32x32x16_bf16 v[80:95], v[198:201], v[6:9], v[80:95]
	v_cvt_scalef32_pk_bf16_fp8 v6, v186, 1.0
	v_cvt_scalef32_pk_bf16_fp8 v7, v186, 1.0 op_sel:[1,0,0]
	v_cvt_scalef32_pk_bf16_fp8 v8, v187, 1.0
	v_cvt_scalef32_pk_bf16_fp8 v9, v187, 1.0 op_sel:[1,0,0]
	ds_read_b128 v[184:187], v0 offset:9248
	v_cvt_pk_f32_fp8_e32 v[14:15], v177
	v_mfma_f32_32x32x16_bf16 v[64:79], v[2:5], v[6:9], v[64:79]
	ds_read_b128 v[2:5], v0 offset:32
	v_mfma_f32_32x32x16_bf16 v[32:47], v[10:13], v[6:9], v[32:47]
	v_mfma_f32_32x32x16_bf16 v[48:63], v[188:191], v[6:9], v[48:63]
	ds_read_b128 v[188:191], v0 offset:13856
	v_mfma_f32_32x32x16_bf16 v[16:31], v[198:201], v[6:9], v[16:31]
	v_cvt_scalef32_pk_bf16_fp8 v6, v180, 1.0
	v_cvt_scalef32_pk_bf16_fp8 v7, v180, 1.0 op_sel:[1,0,0]
	v_cvt_scalef32_pk_bf16_fp8 v8, v181, 1.0
	v_cvt_scalef32_pk_bf16_fp8 v9, v181, 1.0 op_sel:[1,0,0]
	ds_read_b128 v[10:13], v0 offset:4640
	s_waitcnt lgkmcnt(2)
	v_mfma_f32_32x32x16_bf16 v[128:143], v[2:5], v[6:9], v[128:143]
	s_waitcnt lgkmcnt(0)
	v_mfma_f32_32x32x16_bf16 v[96:111], v[10:13], v[6:9], v[96:111]
	v_mfma_f32_32x32x16_bf16 v[112:127], v[184:187], v[6:9], v[112:127]
	v_mfma_f32_32x32x16_bf16 v[80:95], v[188:191], v[6:9], v[80:95]
	v_cvt_pk_f32_fp8_e32 v[6:7], v176
	v_cvt_pk_f32_fp8_sdwa v[8:9], v176 src0_sel:WORD_1
	v_cvt_pk_f32_fp8_sdwa v[176:177], v177 src0_sel:WORD_1
	v_cvt_pk_bf16_f32 v6, v6, v7
	v_cvt_pk_bf16_f32 v7, v8, v9
	v_cvt_pk_bf16_f32 v8, v14, v15
	v_cvt_pk_bf16_f32 v9, v176, v177
	s_nop 1
	v_mfma_f32_32x32x16_bf16 v[64:79], v[2:5], v[6:9], v[64:79]
	ds_read_b128 v[2:5], v0 offset:48
	v_mfma_f32_32x32x16_bf16 v[32:47], v[10:13], v[6:9], v[32:47]
	v_cvt_pk_f32_fp8_e32 v[10:11], v183
	v_cvt_pk_f32_fp8_sdwa v[12:13], v183 src0_sel:WORD_1
	v_mfma_f32_32x32x16_bf16 v[48:63], v[184:187], v[6:9], v[48:63]
	ds_read_b128 v[184:187], v0 offset:13872
	v_mfma_f32_32x32x16_bf16 v[16:31], v[188:191], v[6:9], v[16:31]
	v_cvt_pk_f32_fp8_e32 v[6:7], v182
	v_cvt_pk_f32_fp8_sdwa v[8:9], v182 src0_sel:WORD_1
	ds_read_b128 v[180:183], v0 offset:9264
	v_cvt_pk_bf16_f32 v6, v6, v7
	v_cvt_pk_bf16_f32 v7, v8, v9
	v_cvt_pk_bf16_f32 v8, v10, v11
	v_cvt_pk_bf16_f32 v9, v12, v13
	ds_read_b128 v[10:13], v0 offset:4656
	s_waitcnt lgkmcnt(3)
	v_mfma_f32_32x32x16_bf16 v[128:143], v[2:5], v[6:9], v[128:143]
	s_waitcnt lgkmcnt(0)
	v_mfma_f32_32x32x16_bf16 v[96:111], v[10:13], v[6:9], v[96:111]
	v_mfma_f32_32x32x16_bf16 v[112:127], v[180:183], v[6:9], v[112:127]
	v_mfma_f32_32x32x16_bf16 v[80:95], v[184:187], v[6:9], v[80:95]
	v_cvt_scalef32_pk_bf16_fp8 v6, v178, 1.0
	v_cvt_scalef32_pk_bf16_fp8 v7, v178, 1.0 op_sel:[1,0,0]
	v_cvt_scalef32_pk_bf16_fp8 v8, v179, 1.0
	v_cvt_scalef32_pk_bf16_fp8 v9, v179, 1.0 op_sel:[1,0,0]
	s_nop 1
	v_mfma_f32_32x32x16_bf16 v[64:79], v[2:5], v[6:9], v[64:79]
	v_mfma_f32_32x32x16_bf16 v[32:47], v[10:13], v[6:9], v[32:47]
	v_mfma_f32_32x32x16_bf16 v[48:63], v[180:183], v[6:9], v[48:63]
	v_mfma_f32_32x32x16_bf16 v[16:31], v[184:187], v[6:9], v[16:31]
.LBB0_1326:
	s_and_b32 s98, s2, 0x380
	s_cmp_lt_u32 s49, s40
	s_cselect_b32 s98, s98, 0
	s_add_u32 s98, s98, s54
	s_addc_u32 s99, 0, s55
	global_load_dwordx4 v[180:183], v194, s[98:99] offset:16
	global_load_dwordx4 v[188:191], v194, s[98:99]
	global_load_dwordx4 v[176:179], v195, s[98:99] offset:16
	global_load_dwordx4 v[184:187], v195, s[98:99]
	s_add_i32 s25, s39, 1
	s_cmp_lg_u32 s39, 2
	s_cselect_b32 s29, s25, 0
	s_add_i32 s39, s49, 2
	s_mul_i32 s25, s29, 0x4800
	s_cmp_lt_u32 s39, s40
	v_add_u32_e32 v0, s25, v196
	s_cselect_b32 s25, s39, 0
	s_lshr_b32 s46, s25, 4
	s_add_i32 s46, s46, s76
	s_and_b32 s46, s46, s77
	s_add_i32 s46, s46, s27
	s_lshl_b32 s25, s25, 14
	s_lshl_b32 s46, s46, 6
	s_and_b32 s25, s25, 0x38000
	s_add_i32 s56, s46, s25
	s_waitcnt vmcnt(12)
	v_cvt_pk_bf16_f32 v14, v160, v164
	v_cvt_pk_bf16_f32 v15, v168, v172
	s_lshl_b64 s[46:47], s[56:57], 2
	s_waitcnt lgkmcnt(0)
	s_barrier
	ds_write2_b32 v0, v14, v15 offset1:8
	v_cvt_pk_bf16_f32 v14, v161, v165
	v_cvt_pk_bf16_f32 v15, v169, v173
	v_add_u32_e32 v160, 0x400, v0
	s_add_u32 s46, s11, s46
	ds_write2_b32 v160, v14, v15 offset0:32 offset1:40
	v_cvt_pk_bf16_f32 v14, v162, v166
	v_cvt_pk_bf16_f32 v15, v170, v174
	v_add_u32_e32 v160, 0x800, v0
	s_addc_u32 s47, s79, s47
	ds_write2_b32 v160, v14, v15 offset0:64 offset1:72
	v_cvt_pk_bf16_f32 v14, v163, v167
	v_cvt_pk_bf16_f32 v15, v171, v175
	v_add_u32_e32 v0, 0xc00, v0
	s_add_u32 s90, s46, 0x4000
	ds_write2_b32 v0, v14, v15 offset0:96 offset1:104
	s_addc_u32 s91, s47, 0
	v_mov_b32_e32 v0, v192
	global_load_dwordx4 v[160:163], v0, s[46:47] nt
	global_load_dwordx4 v[164:167], v0, s[46:47] offset:1024 nt
	global_load_dwordx4 v[168:171], v0, s[90:91] nt
	global_load_dwordx4 v[172:175], v0, s[90:91] offset:1024 nt
	s_cmp_ge_u32 s49, s40
	s_cselect_b64 s[46:47], -1, 0
	s_and_b32 s25, s2, 0x380
	s_cmp_lt_u32 s49, s40
	s_cselect_b32 s25, s25, 0
	s_add_u32 s90, s25, s54
	s_addc_u32 s91, 0, s55
	s_and_b64 vcc, exec, s[0:1]
	s_cbranch_vccnz .LBB0_1328
	s_waitcnt vmcnt(14)
	v_add_u32_e32 v0, s26, v197
	ds_read_b128 v[236:239], v0
	v_cvt_scalef32_pk_bf16_fp8 v241, v210, 1.0 op_sel:[1,0,0]
	v_cvt_scalef32_pk_bf16_fp8 v242, v211, 1.0
	ds_read_b128 v[244:247], v0 offset:4608
	ds_read_b128 v[198:201], v0 offset:9216
	ds_read_b128 v[202:205], v0 offset:13824
	v_cvt_scalef32_pk_bf16_fp8 v240, v210, 1.0
	v_cvt_scalef32_pk_bf16_fp8 v243, v211, 1.0 op_sel:[1,0,0]
	s_waitcnt vmcnt(12)
	s_waitcnt lgkmcnt(3)
	v_mfma_f32_32x32x16_bf16 v[128:143], v[236:239], v[240:243], v[128:143]
	s_waitcnt lgkmcnt(2)
	v_mfma_f32_32x32x16_bf16 v[96:111], v[244:247], v[240:243], v[96:111]
	s_waitcnt lgkmcnt(1)
	v_mfma_f32_32x32x16_bf16 v[112:127], v[198:201], v[240:243], v[112:127]
	s_waitcnt lgkmcnt(0)
	v_mfma_f32_32x32x16_bf16 v[80:95], v[202:205], v[240:243], v[80:95]
	v_cvt_scalef32_pk_bf16_fp8 v240, v248, 1.0
	v_cvt_scalef32_pk_bf16_fp8 v241, v248, 1.0 op_sel:[1,0,0]
	v_cvt_scalef32_pk_bf16_fp8 v242, v249, 1.0
	v_cvt_scalef32_pk_bf16_fp8 v243, v249, 1.0 op_sel:[1,0,0]
	s_nop 1
	v_mfma_f32_32x32x16_bf16 v[64:79], v[236:239], v[240:243], v[64:79]
	ds_read_b128 v[236:239], v0 offset:16
	v_cvt_scalef32_pk_bf16_fp8 v232, v212, 1.0
	v_cvt_scalef32_pk_bf16_fp8 v233, v212, 1.0 op_sel:[1,0,0]
	v_cvt_scalef32_pk_bf16_fp8 v10, v250, 1.0
	v_mfma_f32_32x32x16_bf16 v[32:47], v[244:247], v[240:243], v[32:47]
	ds_read_b128 v[244:247], v0 offset:9232
	v_cvt_scalef32_pk_bf16_fp8 v11, v250, 1.0 op_sel:[1,0,0]
	v_mfma_f32_32x32x16_bf16 v[48:63], v[198:201], v[240:243], v[48:63]
	ds_read_b128 v[198:201], v0 offset:13840
	v_mfma_f32_32x32x16_bf16 v[16:31], v[202:205], v[240:243], v[16:31]
	v_cvt_scalef32_pk_bf16_fp8 v234, v213, 1.0
	v_cvt_scalef32_pk_bf16_fp8 v235, v213, 1.0 op_sel:[1,0,0]
	ds_read_b128 v[240:243], v0 offset:4624
	s_waitcnt lgkmcnt(3)
	v_mfma_f32_32x32x16_bf16 v[128:143], v[236:239], v[232:235], v[128:143]
	s_waitcnt lgkmcnt(0)
	v_mfma_f32_32x32x16_bf16 v[96:111], v[240:243], v[232:235], v[96:111]
	v_mfma_f32_32x32x16_bf16 v[112:127], v[244:247], v[232:235], v[112:127]
	v_mfma_f32_32x32x16_bf16 v[80:95], v[198:201], v[232:235], v[80:95]
	v_cvt_scalef32_pk_bf16_fp8 v12, v251, 1.0
	v_cvt_scalef32_pk_bf16_fp8 v13, v251, 1.0 op_sel:[1,0,0]
	ds_read_b128 v[232:235], v0 offset:32
	s_nop 0
	v_mfma_f32_32x32x16_bf16 v[64:79], v[236:239], v[10:13], v[64:79]
	ds_read_b128 v[236:239], v0 offset:4640
	v_mfma_f32_32x32x16_bf16 v[32:47], v[240:243], v[10:13], v[32:47]
	ds_read_b128 v[240:243], v0 offset:9248
	v_mfma_f32_32x32x16_bf16 v[48:63], v[244:247], v[10:13], v[48:63]
	ds_read_b128 v[244:247], v0 offset:13856
	v_mfma_f32_32x32x16_bf16 v[16:31], v[198:201], v[10:13], v[16:31]
	v_cvt_scalef32_pk_bf16_fp8 v10, v206, 1.0
	v_cvt_scalef32_pk_bf16_fp8 v11, v206, 1.0 op_sel:[1,0,0]
	v_cvt_scalef32_pk_bf16_fp8 v12, v207, 1.0
	v_cvt_scalef32_pk_bf16_fp8 v13, v207, 1.0 op_sel:[1,0,0]
	s_waitcnt lgkmcnt(3)
	s_nop 0
	v_mfma_f32_32x32x16_bf16 v[128:143], v[232:235], v[10:13], v[128:143]
	s_waitcnt lgkmcnt(2)
	v_mfma_f32_32x32x16_bf16 v[96:111], v[236:239], v[10:13], v[96:111]
	s_waitcnt lgkmcnt(1)
	v_mfma_f32_32x32x16_bf16 v[112:127], v[240:243], v[10:13], v[112:127]
	s_waitcnt lgkmcnt(0)
	v_mfma_f32_32x32x16_bf16 v[80:95], v[244:247], v[10:13], v[80:95]
	v_cvt_scalef32_pk_bf16_fp8 v10, v214, 1.0
	v_cvt_scalef32_pk_bf16_fp8 v11, v214, 1.0 op_sel:[1,0,0]
	v_cvt_scalef32_pk_bf16_fp8 v12, v215, 1.0
	v_cvt_scalef32_pk_bf16_fp8 v13, v215, 1.0 op_sel:[1,0,0]
	s_nop 1
	v_mfma_f32_32x32x16_bf16 v[64:79], v[232:235], v[10:13], v[64:79]
	ds_read_b128 v[232:235], v0 offset:48
	v_cvt_scalef32_pk_bf16_fp8 v6, v208, 1.0
	v_cvt_scalef32_pk_bf16_fp8 v2, v216, 1.0
	v_mfma_f32_32x32x16_bf16 v[32:47], v[236:239], v[10:13], v[32:47]
	ds_read_b128 v[236:239], v0 offset:9264
	v_mfma_f32_32x32x16_bf16 v[48:63], v[240:243], v[10:13], v[48:63]
	ds_read_b128 v[240:243], v0 offset:13872
	v_mfma_f32_32x32x16_bf16 v[16:31], v[244:247], v[10:13], v[16:31]
	v_cvt_scalef32_pk_bf16_fp8 v9, v209, 1.0 op_sel:[1,0,0]
	v_cvt_scalef32_pk_bf16_fp8 v7, v208, 1.0 op_sel:[1,0,0]
	v_cvt_scalef32_pk_bf16_fp8 v8, v209, 1.0
	ds_read_b128 v[10:13], v0 offset:4656
	s_waitcnt lgkmcnt(3)
	v_mfma_f32_32x32x16_bf16 v[128:143], v[232:235], v[6:9], v[128:143]
	s_waitcnt lgkmcnt(0)
	v_mfma_f32_32x32x16_bf16 v[96:111], v[10:13], v[6:9], v[96:111]
	v_mfma_f32_32x32x16_bf16 v[112:127], v[236:239], v[6:9], v[112:127]
	v_mfma_f32_32x32x16_bf16 v[80:95], v[240:243], v[6:9], v[80:95]
	v_cvt_scalef32_pk_bf16_fp8 v5, v217, 1.0 op_sel:[1,0,0]
	v_cvt_scalef32_pk_bf16_fp8 v3, v216, 1.0 op_sel:[1,0,0]
	v_cvt_scalef32_pk_bf16_fp8 v4, v217, 1.0
	s_nop 1
	v_mfma_f32_32x32x16_bf16 v[64:79], v[232:235], v[2:5], v[64:79]
	v_mfma_f32_32x32x16_bf16 v[32:47], v[10:13], v[2:5], v[32:47]
	v_mfma_f32_32x32x16_bf16 v[48:63], v[236:239], v[2:5], v[48:63]
	v_mfma_f32_32x32x16_bf16 v[16:31], v[240:243], v[2:5], v[16:31]

.LBB0_1433:
	s_add_i32 s25, s87, 1
	s_cmp_lg_u32 s87, 2
	s_cselect_b32 s70, s25, 0
	s_mul_i32 s25, s70, 0x4800
	s_add_i32 s90, s25, 0
	s_add_i32 s25, s88, 1
	s_cmp_lt_u32 s25, s80
	s_cselect_b32 s25, s25, 0
	s_lshr_b32 s42, s25, 2
	s_add_i32 s42, s42, s79
	s_and_b32 s42, s42, s78
	s_add_i32 s42, s42, s77
	s_lshl_b32 s25, s25, 16
	s_lshl_b32 s42, s42, 7
	s_and_b32 s25, s25, 0x30000
	s_add_i32 s56, s42, s25
	v_add_u32_e32 v0, s90, v240
	s_waitcnt vmcnt(5)
	v_cvt_pk_bf16_f32 v2, v160, v164
	s_waitcnt vmcnt(4)
	v_cvt_pk_bf16_f32 v3, v168, v172
	s_lshl_b64 s[42:43], s[56:57], 2
	s_waitcnt lgkmcnt(0)
	s_barrier
	ds_write2_b32 v0, v2, v3 offset1:8
	v_cvt_pk_bf16_f32 v2, v161, v165
	v_cvt_pk_bf16_f32 v3, v169, v173
	v_add_u32_e32 v4, 0x400, v0
	s_add_u32 s42, s82, s42
	ds_write2_b32 v4, v2, v3 offset0:32 offset1:40
	v_cvt_pk_bf16_f32 v2, v162, v166
	v_cvt_pk_bf16_f32 v3, v170, v174
	v_add_u32_e32 v4, 0x800, v0
	s_addc_u32 s43, s83, s43
	ds_write2_b32 v4, v2, v3 offset0:64 offset1:72
	v_cvt_pk_bf16_f32 v2, v163, v167
	v_cvt_pk_bf16_f32 v3, v171, v175
	v_add_u32_e32 v0, 0xc00, v0
	s_add_u32 s68, s42, 0x10000
	ds_write2_b32 v0, v2, v3 offset0:96 offset1:104
	s_addc_u32 s69, s43, 0
	v_mov_b32_e32 v0, v239
	global_load_dwordx4 v[160:163], v0, s[42:43] nt
	global_load_dwordx4 v[168:171], v0, s[68:69] nt
	v_lshl_add_u64 v[2:3], s[42:43], 0, v[0:1]
	v_add_co_u32_e32 v2, vcc, s85, v2
	s_sub_i32 s42, s45, 64
	s_nop 0
	v_addc_co_u32_e32 v3, vcc, 0, v3, vcc
	global_load_dwordx4 v[164:167], v[2:3], off nt
	v_lshl_add_u64 v[2:3], s[68:69], 0, v[0:1]
	v_add_co_u32_e32 v2, vcc, s85, v2
	s_add_i32 s25, s88, -1
	s_nop 0
	v_addc_co_u32_e32 v3, vcc, 0, v3, vcc
	global_load_dwordx4 v[172:175], v[2:3], off nt
	s_and_b32 s42, s42, 0xc0
	s_cmp_lt_u32 s25, s80
	s_cselect_b32 s25, s42, 0
	s_add_u32 s68, s25, s30
	v_cndmask_b32_e64 v0, 0, 1, s[64:65]
	s_addc_u32 s69, 0, s31
	s_mul_i32 s56, s87, 0x4800
	v_cmp_ne_u32_e64 s[42:43], 1, v0
	s_andn2_b64 vcc, exec, s[64:65]
	s_cbranch_vccnz .LBB0_1435
	v_add_u32_e32 v0, s56, v246
	ds_read_b128 v[2:5], v0
	v_cvt_scalef32_pk_bf16_fp8 v6, v212, 1.0
	v_cvt_scalef32_pk_bf16_fp8 v7, v212, 1.0 op_sel:[1,0,0]
	v_cvt_scalef32_pk_bf16_fp8 v8, v213, 1.0
	v_cvt_scalef32_pk_bf16_fp8 v9, v213, 1.0 op_sel:[1,0,0]
	ds_read_b128 v[10:13], v0 offset:4608
	ds_read_b128 v[216:219], v0 offset:9216
	ds_read_b128 v[248:251], v0 offset:13824
	s_waitcnt lgkmcnt(3)
	v_mfma_f32_32x32x16_bf16 v[144:159], v[2:5], v[6:9], v[144:159]
	s_waitcnt vmcnt(6)
	v_cvt_pk_f32_fp8_e32 v[14:15], v209
	s_waitcnt lgkmcnt(2)
	v_mfma_f32_32x32x16_bf16 v[128:143], v[10:13], v[6:9], v[128:143]
	s_waitcnt lgkmcnt(1)
	v_mfma_f32_32x32x16_bf16 v[112:127], v[216:219], v[6:9], v[112:127]
	s_waitcnt lgkmcnt(0)
	v_mfma_f32_32x32x16_bf16 v[96:111], v[248:251], v[6:9], v[96:111]
	v_cvt_pk_f32_fp8_e32 v[6:7], v208
	v_cvt_pk_f32_fp8_sdwa v[8:9], v208 src0_sel:WORD_1
	v_cvt_pk_f32_fp8_sdwa v[208:209], v209 src0_sel:WORD_1
	v_cvt_pk_bf16_f32 v6, v6, v7
	v_cvt_pk_bf16_f32 v7, v8, v9
	v_cvt_pk_bf16_f32 v8, v14, v15
	v_cvt_pk_bf16_f32 v9, v208, v209
	s_nop 1
	v_mfma_f32_32x32x16_bf16 v[80:95], v[2:5], v[6:9], v[80:95]
	ds_read_b128 v[2:5], v0 offset:16
	v_mfma_f32_32x32x16_bf16 v[64:79], v[10:13], v[6:9], v[64:79]
	v_cvt_pk_f32_fp8_e32 v[10:11], v215
	v_cvt_pk_f32_fp8_sdwa v[12:13], v215 src0_sel:WORD_1
	v_mfma_f32_32x32x16_bf16 v[48:63], v[216:219], v[6:9], v[48:63]
	ds_read_b128 v[216:219], v0 offset:13840
	v_mfma_f32_32x32x16_bf16 v[32:47], v[248:251], v[6:9], v[32:47]
	v_cvt_pk_f32_fp8_e32 v[6:7], v214
	v_cvt_pk_f32_fp8_sdwa v[8:9], v214 src0_sel:WORD_1
	ds_read_b128 v[212:215], v0 offset:9232
	v_cvt_pk_bf16_f32 v6, v6, v7
	v_cvt_pk_bf16_f32 v7, v8, v9
	v_cvt_pk_bf16_f32 v8, v10, v11
	v_cvt_pk_bf16_f32 v9, v12, v13
	ds_read_b128 v[10:13], v0 offset:4624
	s_waitcnt lgkmcnt(3)
	v_mfma_f32_32x32x16_bf16 v[144:159], v[2:5], v[6:9], v[144:159]
	s_waitcnt lgkmcnt(0)
	v_mfma_f32_32x32x16_bf16 v[128:143], v[10:13], v[6:9], v[128:143]
	v_mfma_f32_32x32x16_bf16 v[112:127], v[212:215], v[6:9], v[112:127]
	v_mfma_f32_32x32x16_bf16 v[96:111], v[216:219], v[6:9], v[96:111]
	v_cvt_scalef32_pk_bf16_fp8 v6, v210, 1.0
	v_cvt_scalef32_pk_bf16_fp8 v7, v210, 1.0 op_sel:[1,0,0]
	v_cvt_scalef32_pk_bf16_fp8 v8, v211, 1.0
	v_cvt_scalef32_pk_bf16_fp8 v9, v211, 1.0 op_sel:[1,0,0]
	ds_read_b128 v[208:211], v0 offset:9248
	v_cvt_pk_f32_fp8_e32 v[14:15], v193
	v_mfma_f32_32x32x16_bf16 v[80:95], v[2:5], v[6:9], v[80:95]
	ds_read_b128 v[2:5], v0 offset:32
	v_mfma_f32_32x32x16_bf16 v[64:79], v[10:13], v[6:9], v[64:79]
	v_mfma_f32_32x32x16_bf16 v[48:63], v[212:215], v[6:9], v[48:63]
	ds_read_b128 v[212:215], v0 offset:13856
	v_mfma_f32_32x32x16_bf16 v[32:47], v[216:219], v[6:9], v[32:47]
	v_cvt_scalef32_pk_bf16_fp8 v6, v204, 1.0
	v_cvt_scalef32_pk_bf16_fp8 v7, v204, 1.0 op_sel:[1,0,0]
	v_cvt_scalef32_pk_bf16_fp8 v8, v205, 1.0
	v_cvt_scalef32_pk_bf16_fp8 v9, v205, 1.0 op_sel:[1,0,0]
	ds_read_b128 v[10:13], v0 offset:4640
	s_waitcnt lgkmcnt(2)
	v_mfma_f32_32x32x16_bf16 v[144:159], v[2:5], v[6:9], v[144:159]
	s_waitcnt lgkmcnt(0)
	v_mfma_f32_32x32x16_bf16 v[128:143], v[10:13], v[6:9], v[128:143]
	v_mfma_f32_32x32x16_bf16 v[112:127], v[208:211], v[6:9], v[112:127]
	v_mfma_f32_32x32x16_bf16 v[96:111], v[212:215], v[6:9], v[96:111]
	v_cvt_pk_f32_fp8_e32 v[6:7], v192
	v_cvt_pk_f32_fp8_sdwa v[8:9], v192 src0_sel:WORD_1
	v_cvt_pk_f32_fp8_sdwa v[192:193], v193 src0_sel:WORD_1
	v_cvt_pk_bf16_f32 v6, v6, v7
	v_cvt_pk_bf16_f32 v7, v8, v9
	v_cvt_pk_bf16_f32 v8, v14, v15
	v_cvt_pk_bf16_f32 v9, v192, v193
	s_nop 1
	v_mfma_f32_32x32x16_bf16 v[80:95], v[2:5], v[6:9], v[80:95]
	ds_read_b128 v[2:5], v0 offset:48
	v_mfma_f32_32x32x16_bf16 v[64:79], v[10:13], v[6:9], v[64:79]
	v_cvt_pk_f32_fp8_e32 v[10:11], v207
	v_cvt_pk_f32_fp8_sdwa v[12:13], v207 src0_sel:WORD_1
	v_mfma_f32_32x32x16_bf16 v[48:63], v[208:211], v[6:9], v[48:63]
	ds_read_b128 v[208:211], v0 offset:13872
	v_mfma_f32_32x32x16_bf16 v[32:47], v[212:215], v[6:9], v[32:47]
	v_cvt_pk_f32_fp8_e32 v[6:7], v206
	v_cvt_pk_f32_fp8_sdwa v[8:9], v206 src0_sel:WORD_1
	ds_read_b128 v[204:207], v0 offset:9264
	v_cvt_pk_bf16_f32 v6, v6, v7
	v_cvt_pk_bf16_f32 v7, v8, v9
	v_cvt_pk_bf16_f32 v8, v10, v11
	v_cvt_pk_bf16_f32 v9, v12, v13
	ds_read_b128 v[10:13], v0 offset:4656
	s_waitcnt lgkmcnt(3)
	v_mfma_f32_32x32x16_bf16 v[144:159], v[2:5], v[6:9], v[144:159]
	s_waitcnt lgkmcnt(0)
	v_mfma_f32_32x32x16_bf16 v[128:143], v[10:13], v[6:9], v[128:143]
	v_mfma_f32_32x32x16_bf16 v[112:127], v[204:207], v[6:9], v[112:127]
	v_mfma_f32_32x32x16_bf16 v[96:111], v[208:211], v[6:9], v[96:111]
	v_cvt_scalef32_pk_bf16_fp8 v6, v194, 1.0
	v_cvt_scalef32_pk_bf16_fp8 v7, v194, 1.0 op_sel:[1,0,0]
	v_cvt_scalef32_pk_bf16_fp8 v8, v195, 1.0
	v_cvt_scalef32_pk_bf16_fp8 v9, v195, 1.0 op_sel:[1,0,0]
	s_nop 1
	v_mfma_f32_32x32x16_bf16 v[80:95], v[2:5], v[6:9], v[80:95]
	v_mfma_f32_32x32x16_bf16 v[64:79], v[10:13], v[6:9], v[64:79]
	v_mfma_f32_32x32x16_bf16 v[48:63], v[204:207], v[6:9], v[48:63]
	v_mfma_f32_32x32x16_bf16 v[32:47], v[208:211], v[6:9], v[32:47]
.LBB0_1435:
	v_mov_b32_e32 v0, v242
	s_waitcnt vmcnt(5)
	global_load_dwordx4 v[192:195], v0, s[68:69] offset:16
	global_load_dwordx4 v[208:211], v0, s[68:69]
	v_mov_b32_e32 v0, v243
	global_load_dwordx4 v[6:9], v0, s[68:69] offset:16
	global_load_dwordx4 v[204:207], v0, s[68:69]
	v_add_u32_e32 v0, s56, v247
	v_cvt_scalef32_pk_bf16_fp8 v2, v196, 1.0
	v_cvt_scalef32_pk_bf16_fp8 v3, v196, 1.0 op_sel:[1,0,0]
	v_cvt_scalef32_pk_bf16_fp8 v4, v197, 1.0
	v_cvt_scalef32_pk_bf16_fp8 v5, v197, 1.0 op_sel:[1,0,0]
	ds_read_b128 v[10:13], v0
	v_cvt_pk_f32_fp8_sdwa v[14:15], v199 src0_sel:WORD_1
	s_waitcnt lgkmcnt(0)
	v_mfma_f32_32x32x16_bf16 v[16:31], v[10:13], v[2:5], v[16:31]
	v_cvt_pk_f32_fp8_e32 v[12:13], v199
	s_add_i32 s25, s70, 1
	v_cvt_scalef32_pk_bf16_fp8 v10, v198, 1.0
	v_mov_b32_e32 v2, v244
	v_cvt_scalef32_pk_bf16_fp8 v11, v198, 1.0 op_sel:[1,0,0]
	global_load_dwordx4 v[2:5], v2, s[68:69]
	ds_read_b128 v[196:199], v0 offset:16
	ds_read_b128 v[212:215], v0 offset:32
	v_cvt_pk_bf16_f32 v12, v12, v13
	v_cvt_pk_bf16_f32 v13, v14, v15
	s_waitcnt vmcnt(9)
	v_cvt_pk_f32_fp8_e32 v[14:15], v201
	s_cmp_lg_u32 s70, 2
	s_waitcnt lgkmcnt(1)
	v_mfma_f32_32x32x16_bf16 v[16:31], v[196:199], v[10:13], v[16:31]
	v_cvt_pk_f32_fp8_e32 v[10:11], v200
	v_cvt_pk_f32_fp8_sdwa v[12:13], v200 src0_sel:WORD_1
	v_cvt_pk_f32_fp8_sdwa v[196:197], v201 src0_sel:WORD_1
	v_cvt_pk_bf16_f32 v10, v10, v11
	v_cvt_pk_bf16_f32 v11, v12, v13
	v_cvt_pk_bf16_f32 v12, v14, v15
	v_cvt_pk_bf16_f32 v13, v196, v197
	s_cselect_b32 s87, s25, 0
	s_add_i32 s89, s88, 2
	s_waitcnt lgkmcnt(0)
	v_mfma_f32_32x32x16_bf16 v[16:31], v[212:215], v[10:13], v[16:31]
	s_mul_i32 s25, s87, 0x4800
	s_cmp_lt_u32 s89, s80
	v_cvt_pk_f32_fp8_sdwa v[12:13], v202 src0_sel:WORD_1
	v_cvt_scalef32_pk_bf16_fp8 v196, v202, 1.0
	v_mov_b32_e32 v10, v244
	v_cvt_pk_f32_fp8_e32 v[14:15], v203
	v_cvt_scalef32_pk_bf16_fp8 v199, v203, 1.0 op_sel:[1,0,0]
	ds_read_b128 v[200:203], v0 offset:48
	v_add_u32_e32 v0, s25, v245
	s_cselect_b32 s25, s89, 0
	s_lshr_b32 s56, s25, 2
	s_add_i32 s56, s56, s79
	s_and_b32 s56, s56, s78
	s_add_i32 s56, s56, s77
	s_lshl_b32 s25, s25, 16
	s_lshl_b32 s56, s56, 7
	s_and_b32 s25, s25, 0x20000
	s_add_i32 s56, s56, s25
	v_cvt_pk_bf16_f32 v197, v12, v13
	v_cvt_pk_bf16_f32 v198, v14, v15
	global_load_dwordx4 v[10:13], v10, s[68:69] offset:16
	s_waitcnt vmcnt(11)
	v_cvt_pk_bf16_f32 v14, v176, v180
	s_waitcnt vmcnt(10)
	v_cvt_pk_bf16_f32 v15, v184, v188
	s_lshl_b64 s[68:69], s[56:57], 2
	s_waitcnt lgkmcnt(0)
	s_barrier
	ds_write2_b32 v0, v14, v15 offset1:8
	v_cvt_pk_bf16_f32 v14, v177, v181
	v_cvt_pk_bf16_f32 v15, v185, v189
	v_add_u32_e32 v176, 0x400, v0
	s_add_u32 s68, s82, s68
	ds_write2_b32 v176, v14, v15 offset0:32 offset1:40
	v_cvt_pk_bf16_f32 v14, v178, v182
	v_cvt_pk_bf16_f32 v15, v186, v190
	v_add_u32_e32 v176, 0x800, v0
	s_addc_u32 s69, s83, s69
	ds_write2_b32 v176, v14, v15 offset0:64 offset1:72
	v_cvt_pk_bf16_f32 v14, v179, v183
	v_cvt_pk_bf16_f32 v15, v187, v191
	v_add_u32_e32 v0, 0xc00, v0
	s_add_u32 s70, s68, 0x10000
	ds_write2_b32 v0, v14, v15 offset0:96 offset1:104
	s_addc_u32 s71, s69, 0
	v_mov_b32_e32 v0, v239
	global_load_dwordx4 v[176:179], v0, s[68:69] nt
	global_load_dwordx4 v[184:187], v0, s[70:71] nt
	v_lshl_add_u64 v[14:15], s[68:69], 0, v[0:1]
	v_add_co_u32_e32 v14, vcc, s85, v14
	v_mfma_f32_32x32x16_bf16 v[16:31], v[200:203], v[196:199], v[16:31]
	s_nop 0
	v_addc_co_u32_e32 v15, vcc, 0, v15, vcc
	global_load_dwordx4 v[180:183], v[14:15], off nt
	v_lshl_add_u64 v[14:15], s[70:71], 0, v[0:1]
	v_add_co_u32_e32 v14, vcc, s85, v14
	s_cmp_ge_u32 s88, s80
	s_nop 0
	v_addc_co_u32_e32 v15, vcc, 0, v15, vcc
	global_load_dwordx4 v[188:191], v[14:15], off nt
	s_cselect_b64 s[68:69], -1, 0
	s_and_b32 s25, s45, 0x80
	s_cmp_lt_u32 s88, s80
	s_cselect_b32 s25, s25, 0
	s_add_u32 s70, s25, s30
	s_addc_u32 s71, 0, s31
	s_and_b64 vcc, exec, s[42:43]
	s_cbranch_vccnz .LBB0_1437
	s_waitcnt vmcnt(8)
	v_add_u32_e32 v0, s90, v241
	ds_read_b128 v[196:199], v0
	v_cvt_scalef32_pk_bf16_fp8 v201, v208, 1.0 op_sel:[1,0,0]
	v_cvt_scalef32_pk_bf16_fp8 v202, v209, 1.0
	ds_read_b128 v[212:215], v0 offset:4608
	ds_read_b128 v[216:219], v0 offset:9216
	ds_read_b128 v[248:251], v0 offset:13824
	v_cvt_pk_f32_fp8_e32 v[14:15], v208
	v_cvt_pk_f32_fp8_sdwa v[208:209], v209 src0_sel:WORD_1
	v_cvt_pk_bf16_f32 v200, v14, v15
	v_cvt_pk_bf16_f32 v203, v208, v209
	s_waitcnt vmcnt(6)
	v_cvt_pk_f32_fp8_e32 v[14:15], v204
	v_cvt_pk_f32_fp8_e32 v[208:209], v205
	s_waitcnt lgkmcnt(3)
	v_mfma_f32_32x32x16_bf16 v[144:159], v[196:199], v[200:203], v[144:159]
	s_waitcnt lgkmcnt(2)
	v_mfma_f32_32x32x16_bf16 v[128:143], v[212:215], v[200:203], v[128:143]
	s_waitcnt lgkmcnt(1)
	v_mfma_f32_32x32x16_bf16 v[112:127], v[216:219], v[200:203], v[112:127]
	s_waitcnt lgkmcnt(0)
	v_mfma_f32_32x32x16_bf16 v[96:111], v[248:251], v[200:203], v[96:111]
	v_cvt_pk_f32_fp8_sdwa v[202:203], v204 src0_sel:WORD_1
	v_cvt_pk_f32_fp8_sdwa v[204:205], v205 src0_sel:WORD_1
	v_cvt_pk_bf16_f32 v200, v14, v15
	v_cvt_pk_bf16_f32 v201, v202, v203
	v_cvt_pk_bf16_f32 v202, v208, v209
	v_cvt_pk_bf16_f32 v203, v204, v205
	v_cvt_pk_f32_fp8_e32 v[204:205], v211
	s_nop 0
	v_mfma_f32_32x32x16_bf16 v[80:95], v[196:199], v[200:203], v[80:95]
	ds_read_b128 v[196:199], v0 offset:16
	v_mfma_f32_32x32x16_bf16 v[64:79], v[212:215], v[200:203], v[64:79]
	ds_read_b128 v[212:215], v0 offset:9232
	v_mfma_f32_32x32x16_bf16 v[48:63], v[216:219], v[200:203], v[48:63]
	ds_read_b128 v[216:219], v0 offset:13840
	v_mfma_f32_32x32x16_bf16 v[32:47], v[248:251], v[200:203], v[32:47]
	v_cvt_scalef32_pk_bf16_fp8 v200, v210, 1.0
	v_cvt_pk_f32_fp8_e32 v[14:15], v206
	v_cvt_scalef32_pk_bf16_fp8 v201, v210, 1.0 op_sel:[1,0,0]
	v_cvt_scalef32_pk_bf16_fp8 v203, v211, 1.0 op_sel:[1,0,0]
	ds_read_b128 v[208:211], v0 offset:4624
	v_cvt_pk_bf16_f32 v202, v204, v205
	v_cvt_pk_f32_fp8_e32 v[204:205], v207
	s_waitcnt lgkmcnt(3)
	v_mfma_f32_32x32x16_bf16 v[144:159], v[196:199], v[200:203], v[144:159]
	s_waitcnt lgkmcnt(0)
	v_mfma_f32_32x32x16_bf16 v[128:143], v[208:211], v[200:203], v[128:143]
	v_mfma_f32_32x32x16_bf16 v[112:127], v[212:215], v[200:203], v[112:127]
	v_mfma_f32_32x32x16_bf16 v[96:111], v[216:219], v[200:203], v[96:111]
	v_cvt_pk_f32_fp8_sdwa v[202:203], v206 src0_sel:WORD_1
	v_cvt_pk_f32_fp8_sdwa v[206:207], v207 src0_sel:WORD_1
	v_cvt_pk_bf16_f32 v200, v14, v15
	v_cvt_pk_f32_fp8_e32 v[14:15], v192
	v_cvt_pk_bf16_f32 v201, v202, v203
	v_cvt_pk_bf16_f32 v202, v204, v205
	v_cvt_pk_bf16_f32 v203, v206, v207
	v_cvt_pk_f32_fp8_e32 v[204:205], v193
	s_nop 0
	v_mfma_f32_32x32x16_bf16 v[80:95], v[196:199], v[200:203], v[80:95]
	ds_read_b128 v[196:199], v0 offset:32
	v_mfma_f32_32x32x16_bf16 v[64:79], v[208:211], v[200:203], v[64:79]
	ds_read_b128 v[208:211], v0 offset:9248
	v_mfma_f32_32x32x16_bf16 v[48:63], v[212:215], v[200:203], v[48:63]
	ds_read_b128 v[212:215], v0 offset:13856
	v_mfma_f32_32x32x16_bf16 v[32:47], v[216:219], v[200:203], v[32:47]
	v_cvt_pk_f32_fp8_sdwa v[202:203], v192 src0_sel:WORD_1
	v_cvt_pk_f32_fp8_sdwa v[192:193], v193 src0_sel:WORD_1
	v_cvt_pk_bf16_f32 v200, v14, v15
	v_cvt_pk_f32_fp8_e32 v[14:15], v6
	v_cvt_pk_bf16_f32 v201, v202, v203
	v_cvt_pk_bf16_f32 v202, v204, v205
	ds_read_b128 v[204:207], v0 offset:4640
	v_cvt_pk_bf16_f32 v203, v192, v193
	v_cvt_pk_f32_fp8_sdwa v[192:193], v6 src0_sel:WORD_1
	s_waitcnt lgkmcnt(3)
	v_mfma_f32_32x32x16_bf16 v[144:159], v[196:199], v[200:203], v[144:159]
	s_waitcnt lgkmcnt(0)
	v_mfma_f32_32x32x16_bf16 v[128:143], v[204:207], v[200:203], v[128:143]
	v_mfma_f32_32x32x16_bf16 v[112:127], v[208:211], v[200:203], v[112:127]
	v_mfma_f32_32x32x16_bf16 v[96:111], v[212:215], v[200:203], v[96:111]
	v_cvt_pk_f32_fp8_e32 v[202:203], v7
	v_cvt_pk_f32_fp8_sdwa v[6:7], v7 src0_sel:WORD_1
	v_cvt_pk_bf16_f32 v200, v14, v15
	v_cvt_pk_bf16_f32 v201, v192, v193
	v_cvt_pk_bf16_f32 v202, v202, v203
	v_cvt_pk_bf16_f32 v203, v6, v7
	s_nop 1
	v_mfma_f32_32x32x16_bf16 v[80:95], v[196:199], v[200:203], v[80:95]
	ds_read_b128 v[196:199], v0 offset:48
	v_cvt_scalef32_pk_bf16_fp8 v192, v194, 1.0
	v_cvt_scalef32_pk_bf16_fp8 v193, v194, 1.0 op_sel:[1,0,0]
	v_cvt_scalef32_pk_bf16_fp8 v6, v8, 1.0
	v_mfma_f32_32x32x16_bf16 v[64:79], v[204:207], v[200:203], v[64:79]
	ds_read_b128 v[204:207], v0 offset:9264
	v_cvt_scalef32_pk_bf16_fp8 v7, v8, 1.0 op_sel:[1,0,0]
	v_mfma_f32_32x32x16_bf16 v[48:63], v[208:211], v[200:203], v[48:63]
	ds_read_b128 v[208:211], v0 offset:13872
	v_mfma_f32_32x32x16_bf16 v[32:47], v[212:215], v[200:203], v[32:47]
	v_cvt_scalef32_pk_bf16_fp8 v194, v195, 1.0
	v_cvt_scalef32_pk_bf16_fp8 v195, v195, 1.0 op_sel:[1,0,0]
	ds_read_b128 v[200:203], v0 offset:4656
	s_waitcnt lgkmcnt(3)
	v_mfma_f32_32x32x16_bf16 v[144:159], v[196:199], v[192:195], v[144:159]
	s_waitcnt lgkmcnt(0)
	v_mfma_f32_32x32x16_bf16 v[128:143], v[200:203], v[192:195], v[128:143]
	v_mfma_f32_32x32x16_bf16 v[112:127], v[204:207], v[192:195], v[112:127]
	v_mfma_f32_32x32x16_bf16 v[96:111], v[208:211], v[192:195], v[96:111]
	v_cvt_scalef32_pk_bf16_fp8 v8, v9, 1.0
	v_cvt_scalef32_pk_bf16_fp8 v9, v9, 1.0 op_sel:[1,0,0]
	s_nop 1
	v_mfma_f32_32x32x16_bf16 v[80:95], v[196:199], v[6:9], v[80:95]
	v_mfma_f32_32x32x16_bf16 v[64:79], v[200:203], v[6:9], v[64:79]
	v_mfma_f32_32x32x16_bf16 v[48:63], v[204:207], v[6:9], v[48:63]
	v_mfma_f32_32x32x16_bf16 v[32:47], v[208:211], v[6:9], v[32:47]
.LBB0_1437:
	v_mov_b32_e32 v0, v242
	global_load_dwordx4 v[204:207], v0, s[70:71] offset:16
	global_load_dwordx4 v[212:215], v0, s[70:71]
	v_mov_b32_e32 v0, v243
	s_add_i32 s25, s38, s90
	global_load_dwordx4 v[192:195], v0, s[70:71] offset:16
	global_load_dwordx4 v[208:211], v0, s[70:71]
	v_add_u32_e32 v0, s25, v241
	ds_read_b128 v[196:199], v0
	s_waitcnt vmcnt(9)
	v_cvt_pk_f32_fp8_e32 v[6:7], v2
	v_cvt_pk_f32_fp8_sdwa v[8:9], v2 src0_sel:WORD_1
	v_cvt_pk_f32_fp8_e32 v[14:15], v3
	v_cvt_pk_f32_fp8_sdwa v[2:3], v3 src0_sel:WORD_1
	v_cvt_pk_bf16_f32 v6, v6, v7
	v_cvt_pk_bf16_f32 v7, v8, v9
	v_cvt_pk_bf16_f32 v8, v14, v15
	v_cvt_pk_bf16_f32 v9, v2, v3
	s_waitcnt lgkmcnt(0)
	s_nop 0
	v_mfma_f32_32x32x16_bf16 v[16:31], v[196:199], v[6:9], v[16:31]
	v_cvt_pk_f32_fp8_e32 v[8:9], v5
	v_cvt_scalef32_pk_bf16_fp8 v2, v4, 1.0
	v_cvt_scalef32_pk_bf16_fp8 v5, v5, 1.0 op_sel:[1,0,0]
	v_cvt_scalef32_pk_bf16_fp8 v3, v4, 1.0 op_sel:[1,0,0]
	v_mov_b32_e32 v6, v244
	v_cvt_pk_bf16_f32 v4, v8, v9
	global_load_dwordx4 v[196:199], v6, s[70:71]
	ds_read_b128 v[6:9], v0 offset:16
	ds_read_b128 v[200:203], v0 offset:32
	s_waitcnt lgkmcnt(1)
	v_mfma_f32_32x32x16_bf16 v[16:31], v[6:9], v[2:5], v[16:31]
	s_waitcnt vmcnt(9)
	v_cvt_scalef32_pk_bf16_fp8 v2, v10, 1.0
	v_cvt_scalef32_pk_bf16_fp8 v3, v10, 1.0 op_sel:[1,0,0]
	v_cvt_scalef32_pk_bf16_fp8 v4, v11, 1.0
	v_cvt_scalef32_pk_bf16_fp8 v5, v11, 1.0 op_sel:[1,0,0]
	s_waitcnt lgkmcnt(0)
	s_nop 0
	v_mfma_f32_32x32x16_bf16 v[16:31], v[200:203], v[2:5], v[16:31]
	s_add_i32 s56, s88, -2
	s_and_b32 s88, s56, 2
	v_cvt_scalef32_pk_bf16_fp8 v2, v12, 1.0
	v_cvt_scalef32_pk_bf16_fp8 v3, v12, 1.0 op_sel:[1,0,0]
	v_cvt_scalef32_pk_bf16_fp8 v4, v13, 1.0
	v_mov_b32_e32 v6, v244
	global_load_dwordx4 v[200:203], v6, s[70:71] offset:16
	v_cvt_scalef32_pk_bf16_fp8 v5, v13, 1.0 op_sel:[1,0,0]
	ds_read_b128 v[6:9], v0 offset:48
	s_cmp_eq_u32 s88, 0
	s_waitcnt lgkmcnt(0)
	v_mfma_f32_32x32x16_bf16 v[16:31], v[6:9], v[2:5], v[16:31]
	s_cbranch_scc1 .LBB0_1432
	s_lshr_b32 s25, s56, 2
	v_mbcnt_lo_u32_b32 v0, -1, 0
	v_mbcnt_hi_u32_b32 v0, -1, v0
	s_add_i32 s25, s25, s79
	v_and_b32_e32 v248, 31, v0
	v_ashrrev_i32_e32 v0, 5, v0
	s_and_b32 s56, s25, s78
	v_lshlrev_b32_e32 v218, 4, v0
	s_add_i32 s56, s56, s77
	s_and_b64 vcc, exec, s[42:43]
	v_ashrrev_i32_e32 v219, 31, v218
	s_cbranch_vccnz .LBB0_1442
	v_or_b32_e32 v0, s86, v248
	v_lshl_add_u32 v4, v0, 2, 0
	ds_read2st64_b32 v[14:15], v4 offset0:216 offset1:232
	v_mov_b32_e32 v6, v1
	v_mov_b32_e32 v7, v1
	s_lshl_b32 s25, s56, 7
	s_add_u32 s42, s12, s25
	s_waitcnt lgkmcnt(0)
	v_mov_b32_e32 v0, v14
	v_lshlrev_b64 v[216:217], 10, v[0:1]
	v_mul_f32_e32 v0, v144, v15
	v_mul_f32_e32 v5, v148, v15
	v_cvt_pk_fp8_f32 v6, v0, v5
	v_mul_f32_e32 v8, v145, v15
	v_mul_f32_e32 v9, v149, v15
	v_mul_f32_e32 v10, v152, v15
	v_mul_f32_e32 v11, v156, v15
	v_cvt_pk_fp8_f32 v7, v8, v9
	v_cvt_pk_fp8_f32 v6, v10, v11 op_sel:[0,0,1]
	v_mul_f32_e32 v0, v128, v15
	v_mul_f32_e32 v5, v132, v15
	v_mov_b32_e32 v10, v1
	v_cvt_pk_fp8_f32 v10, v0, v5
	v_mul_f32_e32 v12, v153, v15
	v_mul_f32_e32 v13, v157, v15
	v_mul_f32_e32 v14, v146, v15
	v_mul_f32_e32 v144, v150, v15
	v_mul_f32_e32 v147, v147, v15
	v_mul_f32_e32 v148, v151, v15
	v_mov_b32_e32 v8, v1
	v_mov_b32_e32 v9, v1
	v_cvt_pk_fp8_f32 v7, v12, v13 op_sel:[0,0,1]
	v_mul_f32_e32 v12, v129, v15
	v_mul_f32_e32 v13, v133, v15
	v_mov_b32_e32 v11, v1
	v_cvt_pk_fp8_f32 v8, v14, v144
	v_cvt_pk_fp8_f32 v9, v147, v148
	v_mul_f32_e32 v14, v136, v15
	v_mul_f32_e32 v128, v140, v15
	v_mul_f32_e32 v130, v130, v15
	v_mul_f32_e32 v133, v134, v15
	v_mul_f32_e32 v131, v131, v15
	v_mul_f32_e32 v135, v135, v15
	v_cvt_pk_fp8_f32 v11, v12, v13
	v_mov_b32_e32 v12, v1
	v_mov_b32_e32 v13, v1
	v_cvt_pk_fp8_f32 v12, v130, v133
	v_cvt_pk_fp8_f32 v13, v131, v135
	v_cvt_pk_fp8_f32 v10, v14, v128 op_sel:[0,0,1]
	v_mul_f32_e32 v0, v112, v15
	v_mul_f32_e32 v5, v116, v15
	v_mul_f32_e32 v14, v120, v15
	v_mul_f32_e32 v116, v124, v15
	v_mul_f32_e32 v120, v113, v15
	v_mul_f32_e32 v117, v117, v15
	v_mul_f32_e32 v124, v125, v15
	v_mul_f32_e32 v125, v114, v15
	v_mul_f32_e32 v118, v118, v15
	v_mul_f32_e32 v128, v115, v15
	v_mul_f32_e32 v119, v119, v15
	v_mov_b32_e32 v112, v1
	v_mov_b32_e32 v113, v1
	v_mov_b32_e32 v114, v1
	v_mov_b32_e32 v115, v1
	v_cvt_pk_fp8_f32 v112, v0, v5
	v_cvt_pk_fp8_f32 v113, v120, v117
	v_cvt_pk_fp8_f32 v114, v125, v118
	v_cvt_pk_fp8_f32 v115, v128, v119
	v_mul_f32_e32 v145, v154, v15
	v_mul_f32_e32 v146, v158, v15
	v_mul_f32_e32 v149, v155, v15
	v_mul_f32_e32 v150, v159, v15
	v_cvt_pk_fp8_f32 v8, v145, v146 op_sel:[0,0,1]
	v_cvt_pk_fp8_f32 v9, v149, v150 op_sel:[0,0,1]
	v_mul_f32_e32 v129, v137, v15
	v_mul_f32_e32 v132, v141, v15
	v_mul_f32_e32 v134, v138, v15
	v_mul_f32_e32 v136, v142, v15
	v_mul_f32_e32 v137, v139, v15
	v_mul_f32_e32 v138, v143, v15
	s_addc_u32 s43, s13, 0
	v_cvt_pk_fp8_f32 v11, v129, v132 op_sel:[0,0,1]
	v_cvt_pk_fp8_f32 v12, v134, v136 op_sel:[0,0,1]
	v_cvt_pk_fp8_f32 v13, v137, v138 op_sel:[0,0,1]
	v_mul_f32_e32 v121, v121, v15
	v_mul_f32_e32 v122, v122, v15
	v_mul_f32_e32 v126, v126, v15
	v_mul_f32_e32 v123, v123, v15
	v_mul_f32_e32 v127, v127, v15
	v_lshl_add_u64 v[2:3], s[42:43], 0, v[218:219]
	v_cvt_pk_fp8_f32 v112, v14, v116 op_sel:[0,0,1]
	v_cvt_pk_fp8_f32 v113, v121, v124 op_sel:[0,0,1]
	v_cvt_pk_fp8_f32 v114, v122, v126 op_sel:[0,0,1]
	v_cvt_pk_fp8_f32 v115, v123, v127 op_sel:[0,0,1]
	v_lshl_add_u64 v[116:117], v[2:3], 0, v[216:217]
	global_store_dwordx4 v[116:117], v[6:9], off
	global_store_dwordx4 v[116:117], v[10:13], off offset:32
	global_store_dwordx4 v[116:117], v[112:115], off offset:64
	v_mul_f32_e32 v8, v97, v15
	v_mul_f32_e32 v9, v101, v15
	v_mov_b32_e32 v7, v1
	v_mul_f32_e32 v0, v96, v15
	v_mul_f32_e32 v5, v100, v15
	v_mul_f32_e32 v14, v98, v15
	v_mul_f32_e32 v96, v102, v15
	v_mul_f32_e32 v99, v99, v15
	v_mul_f32_e32 v100, v103, v15
	v_mov_b32_e32 v6, v1
	v_cvt_pk_fp8_f32 v7, v8, v9
	v_mov_b32_e32 v8, v1
	v_mov_b32_e32 v9, v1
	v_cvt_pk_fp8_f32 v6, v0, v5
	v_cvt_pk_fp8_f32 v8, v14, v96
	v_cvt_pk_fp8_f32 v9, v99, v100
	v_mul_f32_e32 v10, v104, v15
	v_mul_f32_e32 v11, v108, v15
	v_mul_f32_e32 v12, v105, v15
	v_mul_f32_e32 v13, v109, v15
	v_mul_f32_e32 v97, v106, v15
	v_mul_f32_e32 v98, v110, v15
	v_mul_f32_e32 v101, v107, v15
	v_mul_f32_e32 v15, v111, v15
	v_cvt_pk_fp8_f32 v6, v10, v11 op_sel:[0,0,1]
	v_cvt_pk_fp8_f32 v7, v12, v13 op_sel:[0,0,1]
	v_cvt_pk_fp8_f32 v8, v97, v98 op_sel:[0,0,1]
	v_cvt_pk_fp8_f32 v9, v101, v15 op_sel:[0,0,1]
	s_andn2_b64 vcc, exec, s[66:67]
	global_store_dwordx4 v[116:117], v[6:9], off offset:96
	s_cbranch_vccnz .LBB0_1441
	v_add_u32_e32 v0, 0x80, v4
	ds_read2st64_b32 v[14:15], v0 offset0:216 offset1:232
	s_waitcnt lgkmcnt(0)
	v_mov_b32_e32 v0, v14
	v_lshlrev_b64 v[4:5], 10, v[0:1]
	v_mul_f32_e32 v6, v80, v15
	v_mul_f32_e32 v7, v84, v15
	v_lshl_add_u64 v[96:97], v[2:3], 0, v[4:5]
	v_mov_b32_e32 v2, v1
	v_cvt_pk_fp8_f32 v2, v6, v7
	v_mul_f32_e32 v0, v81, v15
	v_mul_f32_e32 v4, v85, v15
	v_mov_b32_e32 v3, v1
	v_mul_f32_e32 v8, v88, v15
	v_mul_f32_e32 v9, v92, v15
	v_mul_f32_e32 v5, v82, v15
	v_mul_f32_e32 v12, v86, v15
	v_cvt_pk_fp8_f32 v3, v0, v4
	v_mov_b32_e32 v4, v1
	v_mul_f32_e32 v0, v64, v15
	v_mul_f32_e32 v7, v68, v15
	v_mov_b32_e32 v6, v1
	v_cvt_pk_fp8_f32 v4, v5, v12
	v_cvt_pk_fp8_f32 v2, v8, v9 op_sel:[0,0,1]
	v_mul_f32_e32 v8, v65, v15
	v_mul_f32_e32 v9, v69, v15
	v_cvt_pk_fp8_f32 v6, v0, v7
	v_mov_b32_e32 v7, v1
	v_cvt_pk_fp8_f32 v7, v8, v9
	v_mul_f32_e32 v10, v89, v15
	v_mul_f32_e32 v11, v93, v15
	v_mul_f32_e32 v13, v90, v15
	v_mul_f32_e32 v14, v94, v15
	v_cvt_pk_fp8_f32 v3, v10, v11 op_sel:[0,0,1]
	v_mul_f32_e32 v10, v72, v15
	v_mul_f32_e32 v11, v76, v15
	v_cvt_pk_fp8_f32 v4, v13, v14 op_sel:[0,0,1]
	v_mul_f32_e32 v12, v73, v15
	v_mul_f32_e32 v13, v77, v15
	v_cvt_pk_fp8_f32 v6, v10, v11 op_sel:[0,0,1]
	v_mul_f32_e32 v0, v48, v15
	v_mul_f32_e32 v11, v52, v15
	v_mov_b32_e32 v10, v1
	v_cvt_pk_fp8_f32 v7, v12, v13 op_sel:[0,0,1]
	v_mul_f32_e32 v12, v49, v15
	v_mul_f32_e32 v13, v53, v15
	v_cvt_pk_fp8_f32 v10, v0, v11
	v_mov_b32_e32 v11, v1
	v_cvt_pk_fp8_f32 v11, v12, v13
	v_mul_f32_e32 v80, v83, v15
	v_mul_f32_e32 v81, v87, v15
	v_mov_b32_e32 v5, v1
	v_cvt_pk_fp8_f32 v5, v80, v81
	v_mul_f32_e32 v14, v66, v15
	v_mul_f32_e32 v64, v70, v15
	v_mul_f32_e32 v67, v67, v15
	v_mul_f32_e32 v68, v71, v15
	v_mov_b32_e32 v8, v1
	v_mov_b32_e32 v9, v1
	v_cvt_pk_fp8_f32 v8, v14, v64
	v_cvt_pk_fp8_f32 v9, v67, v68
	v_mul_f32_e32 v14, v56, v15
	v_mul_f32_e32 v48, v60, v15
	v_mul_f32_e32 v49, v57, v15
	v_mul_f32_e32 v52, v61, v15
	v_mul_f32_e32 v50, v50, v15
	v_mul_f32_e32 v53, v54, v15
	v_mul_f32_e32 v51, v51, v15
	v_mul_f32_e32 v55, v55, v15
	v_mov_b32_e32 v12, v1
	v_mov_b32_e32 v13, v1
	v_cvt_pk_fp8_f32 v12, v50, v53
	v_cvt_pk_fp8_f32 v13, v51, v55
	v_cvt_pk_fp8_f32 v10, v14, v48 op_sel:[0,0,1]
	v_cvt_pk_fp8_f32 v11, v49, v52 op_sel:[0,0,1]
	v_mul_f32_e32 v0, v32, v15
	v_mul_f32_e32 v14, v36, v15
	v_mul_f32_e32 v36, v40, v15
	v_mul_f32_e32 v40, v44, v15
	v_mul_f32_e32 v44, v33, v15
	v_mul_f32_e32 v37, v37, v15
	v_mul_f32_e32 v48, v34, v15
	v_mul_f32_e32 v38, v38, v15
	v_mul_f32_e32 v49, v35, v15
	v_mul_f32_e32 v39, v39, v15
	v_mov_b32_e32 v32, v1
	v_mov_b32_e32 v33, v1
	v_mov_b32_e32 v34, v1
	v_mov_b32_e32 v35, v1
	v_mul_f32_e32 v82, v91, v15
	v_mul_f32_e32 v83, v95, v15
	v_cvt_pk_fp8_f32 v32, v0, v14
	v_cvt_pk_fp8_f32 v33, v44, v37
	v_cvt_pk_fp8_f32 v34, v48, v38
	v_cvt_pk_fp8_f32 v35, v49, v39
	v_cvt_pk_fp8_f32 v5, v82, v83 op_sel:[0,0,1]
	v_mul_f32_e32 v65, v74, v15
	v_mul_f32_e32 v66, v78, v15
	v_mul_f32_e32 v69, v75, v15
	v_mul_f32_e32 v70, v79, v15
	v_cvt_pk_fp8_f32 v8, v65, v66 op_sel:[0,0,1]
	v_cvt_pk_fp8_f32 v9, v69, v70 op_sel:[0,0,1]
	v_mul_f32_e32 v54, v58, v15
	v_mul_f32_e32 v56, v62, v15
	v_mul_f32_e32 v57, v59, v15
	v_mul_f32_e32 v58, v63, v15
	v_cvt_pk_fp8_f32 v12, v54, v56 op_sel:[0,0,1]
	v_cvt_pk_fp8_f32 v13, v57, v58 op_sel:[0,0,1]
	v_mul_f32_e32 v41, v41, v15
	v_mul_f32_e32 v45, v45, v15
	v_mul_f32_e32 v42, v42, v15
	v_mul_f32_e32 v46, v46, v15
	v_mul_f32_e32 v43, v43, v15
	v_mul_f32_e32 v15, v47, v15
	v_cvt_pk_fp8_f32 v32, v36, v40 op_sel:[0,0,1]
	v_cvt_pk_fp8_f32 v33, v41, v45 op_sel:[0,0,1]
	v_cvt_pk_fp8_f32 v34, v42, v46 op_sel:[0,0,1]
	v_cvt_pk_fp8_f32 v35, v43, v15 op_sel:[0,0,1]
	global_store_dwordx4 v[96:97], v[2:5], off
	global_store_dwordx4 v[96:97], v[6:9], off offset:32
	global_store_dwordx4 v[96:97], v[10:13], off offset:64
	global_store_dwordx4 v[96:97], v[32:35], off offset:96
